# nt also on the stores of the prologue x pass and the combine phases
# speedup vs baseline: 1.0007x; 1.0007x over previous
.LBB0_154:
	s_waitcnt vmcnt(7)
	v_mul_f32_e32 v80, v1, v1
	v_mul_f32_e32 v81, v3, v3
	v_fmac_f32_e32 v80, v0, v0
	v_fmac_f32_e32 v81, v2, v2
	v_add_f32_e32 v80, v80, v81
	s_waitcnt vmcnt(6)
	v_mul_f32_e32 v81, v5, v5
	v_mul_f32_e32 v82, v7, v7
	v_fmac_f32_e32 v81, v4, v4
	v_fmac_f32_e32 v82, v6, v6
	v_add_f32_e32 v81, v81, v82
	v_add_f32_e32 v80, v80, v81
	s_waitcnt vmcnt(5)
	v_mul_f32_e32 v81, v9, v9
	v_mul_f32_e32 v82, v11, v11
	v_fmac_f32_e32 v81, v8, v8
	v_fmac_f32_e32 v82, v10, v10
	v_add_f32_e32 v81, v81, v82
	v_add_f32_e32 v80, v81, v80
	s_waitcnt vmcnt(4)
	v_mul_f32_e32 v81, v13, v13
	v_mul_f32_e32 v82, v15, v15
	v_fmac_f32_e32 v81, v12, v12
	v_fmac_f32_e32 v82, v14, v14
	v_add_f32_e32 v81, v81, v82
	v_add_f32_e32 v80, v81, v80
	s_waitcnt vmcnt(3)
	v_mul_f32_e32 v81, v17, v17
	v_mul_f32_e32 v82, v19, v19
	v_fmac_f32_e32 v81, v16, v16
	v_fmac_f32_e32 v82, v18, v18
	v_add_f32_e32 v81, v81, v82
	v_add_f32_e32 v80, v81, v80
	s_waitcnt vmcnt(2)
	v_mul_f32_e32 v81, v21, v21
	v_mul_f32_e32 v82, v23, v23
	v_fmac_f32_e32 v81, v20, v20
	v_fmac_f32_e32 v82, v22, v22
	v_add_f32_e32 v81, v81, v82
	v_add_f32_e32 v80, v81, v80
	s_waitcnt vmcnt(1)
	v_mul_f32_e32 v81, v25, v25
	v_mul_f32_e32 v82, v27, v27
	v_fmac_f32_e32 v81, v24, v24
	v_fmac_f32_e32 v82, v26, v26
	v_add_f32_e32 v81, v81, v82
	v_add_f32_e32 v80, v81, v80
	s_waitcnt vmcnt(0)
	v_mul_f32_e32 v81, v29, v29
	v_mul_f32_e32 v82, v31, v31
	v_fmac_f32_e32 v81, v28, v28
	v_fmac_f32_e32 v82, v30, v30
	v_add_f32_e32 v81, v81, v82
	v_add_f32_e32 v80, v81, v80
	ds_bpermute_b32 v81, v73, v80
	v_max_f32_e64 v84, |v3|, |v3|
	v_max_f32_e64 v85, |v2|, |v2|
	v_max_f32_e32 v84, v85, v84
	v_max_f32_e64 v85, |v7|, |v7|
	s_waitcnt lgkmcnt(0)
	v_add_f32_e32 v80, v80, v81
	ds_bpermute_b32 v81, v74, v80
	v_max_f32_e64 v86, |v6|, |v6|
	v_max_f32_e32 v85, v86, v85
	v_max3_f32 v84, |v0|, |v1|, v84
	v_max3_f32 v85, |v4|, |v5|, v85
	s_waitcnt lgkmcnt(0)
	v_add_f32_e32 v80, v80, v81
	ds_bpermute_b32 v81, v75, v80
	v_max3_f32 v84, v84, 0, v85
	v_max_f32_e64 v85, |v11|, |v11|
	v_max_f32_e64 v86, |v10|, |v10|
	v_max_f32_e32 v85, v86, v85
	s_waitcnt lgkmcnt(0)
	v_add_f32_e32 v80, v80, v81
	ds_bpermute_b32 v81, v76, v80
	v_max_f32_e64 v86, |v15|, |v15|
	v_max_f32_e64 v87, |v14|, |v14|
	v_max_f32_e32 v86, v87, v86
	v_max3_f32 v85, |v8|, |v9|, v85
	s_waitcnt lgkmcnt(0)
	v_add_f32_e32 v80, v80, v81
	ds_bpermute_b32 v81, v77, v80
	v_max3_f32 v86, |v12|, |v13|, v86
	v_max3_f32 v84, v84, v85, v86
	v_max_f32_e64 v85, |v19|, |v19|
	v_max_f32_e64 v86, |v18|, |v18|
	s_waitcnt lgkmcnt(0)
	v_add_f32_e32 v80, v80, v81
	ds_bpermute_b32 v81, v78, v80
	v_max_f32_e32 v85, v86, v85
	v_max_f32_e64 v86, |v23|, |v23|
	v_max_f32_e64 v87, |v22|, |v22|
	v_max_f32_e32 v86, v87, v86
	v_max3_f32 v85, |v16|, |v17|, v85
	v_max3_f32 v86, |v20|, |v21|, v86
	v_max3_f32 v84, v84, v85, v86
	v_max_f32_e64 v85, |v27|, |v27|
	v_max_f32_e64 v86, |v26|, |v26|
	v_max_f32_e32 v85, v86, v85
	v_max_f32_e64 v86, |v31|, |v31|
	v_max_f32_e64 v87, |v30|, |v30|
	s_waitcnt lgkmcnt(0)
	v_add_f32_e32 v80, v80, v81
	v_max_f32_e32 v86, v87, v86
	v_fmamk_f32 v80, v80, 0x3a000000, v64
	v_max3_f32 v85, |v24|, |v25|, v85
	v_max3_f32 v86, |v28|, |v29|, v86
	v_mul_f32_e32 v81, 0x4f800000, v80
	v_cmp_gt_f32_e32 vcc, s15, v80
	v_max3_f32 v84, v84, v85, v86
	ds_bpermute_b32 v85, v73, v84
	v_cndmask_b32_e32 v80, v80, v81, vcc
	v_sqrt_f32_e32 v81, v80
	s_ashr_i32 s7, s6, 31
	s_lshl_b64 s[18:19], s[6:7], 12
	s_waitcnt lgkmcnt(0)
	v_max_f32_e32 v85, v85, v85
	v_add_u32_e32 v82, -1, v81
	v_fma_f32 v83, -v82, v81, v80
	v_max_f32_e32 v84, v84, v85
	v_cmp_ge_f32_e64 s[4:5], 0, v83
	v_add_u32_e32 v83, 1, v81
	ds_bpermute_b32 v85, v74, v84
	v_cndmask_b32_e64 v82, v81, v82, s[4:5]
	v_fma_f32 v81, -v83, v81, v80
	v_cmp_lt_f32_e64 s[4:5], 0, v81
	v_cvt_pk_bf16_f32 v88, v0, v1
	v_cvt_pk_bf16_f32 v89, v2, v3
	s_nop 1
	v_cndmask_b32_e64 v81, v82, v83, s[4:5]
	v_mul_f32_e32 v82, 0x37800000, v81
	v_cndmask_b32_e32 v81, v81, v82, vcc
	s_waitcnt lgkmcnt(0)
	v_max_f32_e32 v82, v85, v85
	v_max_f32_e32 v82, v84, v82
	ds_bpermute_b32 v83, v75, v82
	v_cmp_class_f32_e32 vcc, v80, v79
	s_waitcnt lgkmcnt(0)
	v_max_f32_e32 v83, v83, v83
	v_max_f32_e32 v82, v82, v83
	ds_bpermute_b32 v83, v76, v82
	v_cndmask_b32_e32 v80, v81, v80, vcc
	v_div_scale_f32 v81, s[4:5], v80, v80, 1.0
	v_rcp_f32_e32 v84, v81
	s_waitcnt lgkmcnt(0)
	v_max_f32_e32 v83, v83, v83
	v_max_f32_e32 v82, v82, v83
	ds_bpermute_b32 v83, v77, v82
	v_fma_f32 v85, -v81, v84, 1.0
	v_fmac_f32_e32 v84, v85, v84
	v_div_scale_f32 v85, vcc, 1.0, v80, 1.0
	s_waitcnt lgkmcnt(0)
	v_max_f32_e32 v83, v83, v83
	v_max_f32_e32 v82, v82, v83
	v_mul_f32_e32 v86, v85, v84
	ds_bpermute_b32 v83, v78, v82
	v_fma_f32 v87, -v81, v86, v85
	v_fmac_f32_e32 v86, v87, v84
	v_fma_f32 v81, -v81, v86, v85
	v_div_fmas_f32 v81, v81, v84, v86
	v_div_fixup_f32 v81, v81, v80, 1.0
	s_waitcnt lgkmcnt(0)
	v_max_f32_e32 v80, v83, v83
	v_max_f32_e32 v80, v82, v80
	v_mul_f32_e32 v80, v81, v80
	v_max_f32_e32 v80, 0x1e3ce508, v80
	v_mul_f32_e32 v81, 0x42fe0000, v81
	v_div_scale_f32 v82, s[4:5], v80, v80, v81
	v_rcp_f32_e32 v83, v82
	s_lshl_b64 s[4:5], s[6:7], 11
	v_fma_f32 v84, -v82, v83, 1.0
	v_fmac_f32_e32 v83, v84, v83
	v_div_scale_f32 v84, vcc, v81, v80, v81
	v_mul_f32_e32 v85, v84, v83
	v_fma_f32 v86, -v82, v85, v84
	v_fmac_f32_e32 v85, v86, v83
	v_fma_f32 v82, -v82, v85, v84
	v_div_fmas_f32 v82, v82, v83, v85
	v_div_fixup_f32 v82, v82, v80, v81
	v_lshl_add_u64 v[84:85], v[66:67], 0, s[18:19]
	v_pk_mul_f32 v[90:91], v[0:1], v[82:83] op_sel_hi:[1,0]
	global_store_dwordx2 v[84:85], v[88:89], off nt
	v_pk_mul_f32 v[88:89], v[2:3], v[82:83] op_sel_hi:[1,0]
	v_rndne_f32_e32 v83, v91
	v_rndne_f32_e32 v81, v90
	v_cvt_i32_f32_e32 v83, v83
	v_rndne_f32_e32 v88, v88
	v_rndne_f32_e32 v89, v89
	v_cvt_i32_f32_e32 v81, v81
	v_cvt_i32_f32_sdwa v88, v88 dst_sel:WORD_1 dst_unused:UNUSED_PAD src0_sel:DWORD
	v_cvt_i32_f32_e32 v89, v89
	v_lshlrev_b32_e32 v83, 8, v83
	v_and_b32_e32 v83, 0xff00, v83
	v_and_b32_e32 v88, 0xff0000, v88
	v_perm_b32 v81, v89, v81, s16
	v_lshl_add_u64 v[86:87], v[68:69], 0, s[4:5]
	v_or3_b32 v81, v81, v83, v88
	global_store_dword v[86:87], v81, off nt
	v_cvt_pk_bf16_f32 v88, v4, v5
	v_cvt_pk_bf16_f32 v89, v6, v7
	v_pk_mul_f32 v[90:91], v[4:5], v[82:83] op_sel_hi:[1,0]
	global_store_dwordx2 v[84:85], v[88:89], off offset:512 nt
	v_pk_mul_f32 v[88:89], v[6:7], v[82:83] op_sel_hi:[1,0]
	v_rndne_f32_e32 v83, v91
	v_rndne_f32_e32 v81, v90
	v_cvt_i32_f32_e32 v83, v83
	v_rndne_f32_e32 v88, v88
	v_rndne_f32_e32 v89, v89
	v_cvt_i32_f32_e32 v81, v81
	v_cvt_i32_f32_sdwa v88, v88 dst_sel:WORD_1 dst_unused:UNUSED_PAD src0_sel:DWORD
	v_cvt_i32_f32_e32 v89, v89
	v_lshlrev_b32_e32 v83, 8, v83
	v_and_b32_e32 v83, 0xff00, v83
	v_and_b32_e32 v88, 0xff0000, v88
	v_perm_b32 v81, v89, v81, s16
	v_or3_b32 v81, v81, v83, v88
	global_store_dword v[86:87], v81, off offset:256 nt
	v_cvt_pk_bf16_f32 v88, v8, v9
	v_cvt_pk_bf16_f32 v89, v10, v11
	v_pk_mul_f32 v[90:91], v[8:9], v[82:83] op_sel_hi:[1,0]
	global_store_dwordx2 v[84:85], v[88:89], off offset:1024 nt
	v_pk_mul_f32 v[88:89], v[10:11], v[82:83] op_sel_hi:[1,0]
	v_rndne_f32_e32 v83, v91
	v_rndne_f32_e32 v81, v90
	v_cvt_i32_f32_e32 v83, v83
	v_rndne_f32_e32 v88, v88
	v_rndne_f32_e32 v89, v89
	v_cvt_i32_f32_e32 v81, v81
	v_cvt_i32_f32_sdwa v88, v88 dst_sel:WORD_1 dst_unused:UNUSED_PAD src0_sel:DWORD
	v_cvt_i32_f32_e32 v89, v89
	v_lshlrev_b32_e32 v83, 8, v83
	v_and_b32_e32 v83, 0xff00, v83
	v_and_b32_e32 v88, 0xff0000, v88
	v_perm_b32 v81, v89, v81, s16
	v_or3_b32 v81, v81, v83, v88
	global_store_dword v[86:87], v81, off offset:512 nt
	v_cvt_pk_bf16_f32 v88, v12, v13
	v_cvt_pk_bf16_f32 v89, v14, v15
	v_pk_mul_f32 v[90:91], v[12:13], v[82:83] op_sel_hi:[1,0]
	global_store_dwordx2 v[84:85], v[88:89], off offset:1536 nt
	v_pk_mul_f32 v[88:89], v[14:15], v[82:83] op_sel_hi:[1,0]
	v_rndne_f32_e32 v83, v91
	v_rndne_f32_e32 v81, v90
	v_cvt_i32_f32_e32 v83, v83
	v_rndne_f32_e32 v88, v88
	v_rndne_f32_e32 v89, v89
	v_cvt_i32_f32_e32 v81, v81
	v_cvt_i32_f32_sdwa v88, v88 dst_sel:WORD_1 dst_unused:UNUSED_PAD src0_sel:DWORD
	v_cvt_i32_f32_e32 v89, v89
	v_lshlrev_b32_e32 v83, 8, v83
	v_and_b32_e32 v83, 0xff00, v83
	v_and_b32_e32 v88, 0xff0000, v88
	v_perm_b32 v81, v89, v81, s16
	v_or3_b32 v81, v81, v83, v88
	global_store_dword v[86:87], v81, off offset:768 nt
	v_cvt_pk_bf16_f32 v88, v16, v17
	v_cvt_pk_bf16_f32 v89, v18, v19
	v_pk_mul_f32 v[90:91], v[16:17], v[82:83] op_sel_hi:[1,0]
	global_store_dwordx2 v[84:85], v[88:89], off offset:2048 nt
	v_pk_mul_f32 v[88:89], v[18:19], v[82:83] op_sel_hi:[1,0]
	v_rndne_f32_e32 v83, v91
	v_rndne_f32_e32 v81, v90
	v_cvt_i32_f32_e32 v83, v83
	v_rndne_f32_e32 v88, v88
	v_rndne_f32_e32 v89, v89
	v_cvt_i32_f32_e32 v81, v81
	v_cvt_i32_f32_sdwa v88, v88 dst_sel:WORD_1 dst_unused:UNUSED_PAD src0_sel:DWORD
	v_cvt_i32_f32_e32 v89, v89
	v_lshlrev_b32_e32 v83, 8, v83
	v_and_b32_e32 v83, 0xff00, v83
	v_and_b32_e32 v88, 0xff0000, v88
	v_perm_b32 v81, v89, v81, s16
	v_or3_b32 v81, v81, v83, v88
	global_store_dword v[86:87], v81, off offset:1024 nt
	v_cvt_pk_bf16_f32 v88, v20, v21
	v_cvt_pk_bf16_f32 v89, v22, v23
	v_pk_mul_f32 v[90:91], v[20:21], v[82:83] op_sel_hi:[1,0]
	global_store_dwordx2 v[84:85], v[88:89], off offset:2560 nt
	v_pk_mul_f32 v[88:89], v[22:23], v[82:83] op_sel_hi:[1,0]
	v_rndne_f32_e32 v83, v91
	v_rndne_f32_e32 v81, v90
	v_cvt_i32_f32_e32 v83, v83
	v_rndne_f32_e32 v88, v88
	v_rndne_f32_e32 v89, v89
	v_cvt_i32_f32_e32 v81, v81
	v_cvt_i32_f32_sdwa v88, v88 dst_sel:WORD_1 dst_unused:UNUSED_PAD src0_sel:DWORD
	v_cvt_i32_f32_e32 v89, v89
	v_lshlrev_b32_e32 v83, 8, v83
	v_and_b32_e32 v83, 0xff00, v83
	v_and_b32_e32 v88, 0xff0000, v88
	v_perm_b32 v81, v89, v81, s16
	v_or3_b32 v81, v81, v83, v88
	global_store_dword v[86:87], v81, off offset:1280 nt
	v_cvt_pk_bf16_f32 v88, v24, v25
	v_cvt_pk_bf16_f32 v89, v26, v27
	v_pk_mul_f32 v[90:91], v[24:25], v[82:83] op_sel_hi:[1,0]
	global_store_dwordx2 v[84:85], v[88:89], off offset:3072 nt
	v_pk_mul_f32 v[88:89], v[26:27], v[82:83] op_sel_hi:[1,0]
	v_rndne_f32_e32 v83, v91
	v_rndne_f32_e32 v81, v90
	v_cvt_i32_f32_e32 v83, v83
	v_rndne_f32_e32 v88, v88
	v_rndne_f32_e32 v89, v89
	v_cvt_i32_f32_e32 v81, v81
	v_cvt_i32_f32_sdwa v88, v88 dst_sel:WORD_1 dst_unused:UNUSED_PAD src0_sel:DWORD
	v_cvt_i32_f32_e32 v89, v89
	v_lshlrev_b32_e32 v83, 8, v83
	v_and_b32_e32 v83, 0xff00, v83
	v_and_b32_e32 v88, 0xff0000, v88
	v_perm_b32 v81, v89, v81, s16
	v_or3_b32 v81, v81, v83, v88
	global_store_dword v[86:87], v81, off offset:1536 nt
	v_cvt_pk_bf16_f32 v88, v28, v29
	v_cvt_pk_bf16_f32 v89, v30, v31
	global_store_dwordx2 v[84:85], v[88:89], off offset:3584 nt
	v_pk_mul_f32 v[84:85], v[30:31], v[82:83] op_sel_hi:[1,0]
	v_pk_mul_f32 v[82:83], v[28:29], v[82:83] op_sel_hi:[1,0]
	s_nop 0
	v_rndne_f32_e32 v81, v82
	v_rndne_f32_e32 v82, v83
	v_cvt_i32_f32_e32 v82, v82
	v_rndne_f32_e32 v83, v84
	v_rndne_f32_e32 v84, v85
	v_cvt_i32_f32_e32 v81, v81
	v_cvt_i32_f32_sdwa v83, v83 dst_sel:WORD_1 dst_unused:UNUSED_PAD src0_sel:DWORD
	v_cvt_i32_f32_e32 v84, v84
	v_lshlrev_b32_e32 v82, 8, v82
	v_and_b32_e32 v82, 0xff00, v82
	v_and_b32_e32 v83, 0xff0000, v83
	v_perm_b32 v81, v84, v81, s16
	v_or3_b32 v81, v81, v82, v83
	global_store_dword v[86:87], v81, off offset:1792 nt
	s_and_saveexec_b64 s[4:5], s[0:1]
	s_cbranch_execz .LBB0_156
	s_lshl_b64 s[18:19], s[6:7], 2
	s_add_u32 s18, s11, s18
	s_addc_u32 s19, s14, s19
	v_mul_f32_e32 v80, 0x3c010204, v80
	global_store_dword v65, v80, s[18:19] nt
	s_or_b64 exec, exec, s[4:5]
	s_andn2_b64 vcc, exec, s[8:9]
	s_mov_b64 s[8:9], 0
	s_cbranch_vccnz .LBB0_151
	s_branch .LBB0_157

.LBB0_159:
	v_mul_f32_e32 v80, v45, v45
	v_mul_f32_e32 v81, v47, v47
	v_fmac_f32_e32 v80, v44, v44
	v_fmac_f32_e32 v81, v46, v46
	v_add_f32_e32 v80, v80, v81
	v_mul_f32_e32 v81, v41, v41
	v_mul_f32_e32 v82, v43, v43
	v_fmac_f32_e32 v81, v40, v40
	v_fmac_f32_e32 v82, v42, v42
	v_add_f32_e32 v81, v81, v82
	v_add_f32_e32 v80, v81, v80
	v_mul_f32_e32 v81, v37, v37
	v_mul_f32_e32 v82, v39, v39
	v_fmac_f32_e32 v81, v36, v36
	v_fmac_f32_e32 v82, v38, v38
	v_add_f32_e32 v81, v81, v82
	v_add_f32_e32 v80, v81, v80
	v_mul_f32_e32 v81, v33, v33
	v_mul_f32_e32 v82, v35, v35
	v_fmac_f32_e32 v81, v32, v32
	v_fmac_f32_e32 v82, v34, v34
	v_add_f32_e32 v81, v81, v82
	v_add_f32_e32 v80, v81, v80
	v_mul_f32_e32 v81, v61, v61
	v_mul_f32_e32 v82, v63, v63
	v_fmac_f32_e32 v81, v60, v60
	v_fmac_f32_e32 v82, v62, v62
	v_add_f32_e32 v81, v81, v82
	v_add_f32_e32 v80, v81, v80
	v_mul_f32_e32 v81, v57, v57
	v_mul_f32_e32 v82, v59, v59
	v_fmac_f32_e32 v81, v56, v56
	v_fmac_f32_e32 v82, v58, v58
	v_add_f32_e32 v81, v81, v82
	v_add_f32_e32 v80, v81, v80
	v_mul_f32_e32 v81, v53, v53
	v_mul_f32_e32 v82, v55, v55
	v_fmac_f32_e32 v81, v52, v52
	v_fmac_f32_e32 v82, v54, v54
	v_add_f32_e32 v81, v81, v82
	v_add_f32_e32 v80, v81, v80
	v_mul_f32_e32 v81, v49, v49
	v_mul_f32_e32 v82, v51, v51
	v_fmac_f32_e32 v81, v48, v48
	v_fmac_f32_e32 v82, v50, v50
	v_add_f32_e32 v81, v81, v82
	v_add_f32_e32 v80, v81, v80
	ds_bpermute_b32 v81, v73, v80
	v_max_f32_e64 v84, |v47|, |v47|
	v_max_f32_e64 v85, |v46|, |v46|
	v_max_f32_e32 v84, v85, v84
	v_max_f32_e64 v85, |v43|, |v43|
	s_waitcnt lgkmcnt(0)
	v_add_f32_e32 v80, v80, v81
	ds_bpermute_b32 v81, v74, v80
	v_max_f32_e64 v86, |v42|, |v42|
	v_max_f32_e32 v85, v86, v85
	v_max3_f32 v84, |v44|, |v45|, v84
	v_max3_f32 v85, |v40|, |v41|, v85
	s_waitcnt lgkmcnt(0)
	v_add_f32_e32 v80, v80, v81
	ds_bpermute_b32 v81, v75, v80
	v_max3_f32 v84, v84, 0, v85
	v_max_f32_e64 v85, |v39|, |v39|
	v_max_f32_e64 v86, |v38|, |v38|
	v_max_f32_e32 v85, v86, v85
	s_waitcnt lgkmcnt(0)
	v_add_f32_e32 v80, v80, v81
	ds_bpermute_b32 v81, v76, v80
	v_max_f32_e64 v86, |v35|, |v35|
	v_max_f32_e64 v87, |v34|, |v34|
	v_max_f32_e32 v86, v87, v86
	v_max3_f32 v85, |v36|, |v37|, v85
	s_waitcnt lgkmcnt(0)
	v_add_f32_e32 v80, v80, v81
	ds_bpermute_b32 v81, v77, v80
	v_max3_f32 v86, |v32|, |v33|, v86
	v_max3_f32 v84, v84, v85, v86
	v_max_f32_e64 v85, |v63|, |v63|
	v_max_f32_e64 v86, |v62|, |v62|
	s_waitcnt lgkmcnt(0)
	v_add_f32_e32 v80, v80, v81
	ds_bpermute_b32 v81, v78, v80
	v_max_f32_e32 v85, v86, v85
	v_max_f32_e64 v86, |v59|, |v59|
	v_max_f32_e64 v87, |v58|, |v58|
	v_max_f32_e32 v86, v87, v86
	v_max3_f32 v85, |v60|, |v61|, v85
	v_max3_f32 v86, |v56|, |v57|, v86
	v_max3_f32 v84, v84, v85, v86
	v_max_f32_e64 v85, |v55|, |v55|
	v_max_f32_e64 v86, |v54|, |v54|
	v_max_f32_e32 v85, v86, v85
	v_max_f32_e64 v86, |v51|, |v51|
	v_max_f32_e64 v87, |v50|, |v50|
	s_waitcnt lgkmcnt(0)
	v_add_f32_e32 v80, v80, v81
	v_max_f32_e32 v86, v87, v86
	v_fmamk_f32 v80, v80, 0x3a000000, v64
	v_max3_f32 v85, |v52|, |v53|, v85
	v_max3_f32 v86, |v48|, |v49|, v86
	v_mul_f32_e32 v81, 0x4f800000, v80
	v_cmp_gt_f32_e32 vcc, s15, v80
	v_max3_f32 v84, v84, v85, v86
	ds_bpermute_b32 v85, v73, v84
	v_cndmask_b32_e32 v80, v80, v81, vcc
	v_sqrt_f32_e32 v81, v80
	s_ashr_i32 s3, s2, 31
	s_lshl_b64 s[18:19], s[2:3], 12
	s_waitcnt lgkmcnt(0)
	v_max_f32_e32 v85, v85, v85
	v_add_u32_e32 v82, -1, v81
	v_fma_f32 v83, -v82, v81, v80
	v_max_f32_e32 v84, v84, v85
	v_cmp_ge_f32_e64 s[4:5], 0, v83
	v_add_u32_e32 v83, 1, v81
	ds_bpermute_b32 v85, v74, v84
	v_cndmask_b32_e64 v82, v81, v82, s[4:5]
	v_fma_f32 v81, -v83, v81, v80
	v_cmp_lt_f32_e64 s[4:5], 0, v81
	v_cvt_pk_bf16_f32 v88, v44, v45
	v_cvt_pk_bf16_f32 v89, v46, v47
	s_nop 1
	v_cndmask_b32_e64 v81, v82, v83, s[4:5]
	v_mul_f32_e32 v82, 0x37800000, v81
	v_cndmask_b32_e32 v81, v81, v82, vcc
	s_waitcnt lgkmcnt(0)
	v_max_f32_e32 v82, v85, v85
	v_max_f32_e32 v82, v84, v82
	ds_bpermute_b32 v83, v75, v82
	v_cmp_class_f32_e32 vcc, v80, v79
	s_waitcnt lgkmcnt(0)
	v_max_f32_e32 v83, v83, v83
	v_max_f32_e32 v82, v82, v83
	ds_bpermute_b32 v83, v76, v82
	v_cndmask_b32_e32 v80, v81, v80, vcc
	v_div_scale_f32 v81, s[4:5], v80, v80, 1.0
	v_rcp_f32_e32 v84, v81
	s_waitcnt lgkmcnt(0)
	v_max_f32_e32 v83, v83, v83
	v_max_f32_e32 v82, v82, v83
	ds_bpermute_b32 v83, v77, v82
	v_fma_f32 v85, -v81, v84, 1.0
	v_fmac_f32_e32 v84, v85, v84
	v_div_scale_f32 v85, vcc, 1.0, v80, 1.0
	s_waitcnt lgkmcnt(0)
	v_max_f32_e32 v83, v83, v83
	v_max_f32_e32 v82, v82, v83
	v_mul_f32_e32 v86, v85, v84
	ds_bpermute_b32 v83, v78, v82
	v_fma_f32 v87, -v81, v86, v85
	v_fmac_f32_e32 v86, v87, v84
	v_fma_f32 v81, -v81, v86, v85
	v_div_fmas_f32 v81, v81, v84, v86
	v_div_fixup_f32 v81, v81, v80, 1.0
	s_waitcnt lgkmcnt(0)
	v_max_f32_e32 v80, v83, v83
	v_max_f32_e32 v80, v82, v80
	v_mul_f32_e32 v80, v81, v80
	v_max_f32_e32 v80, 0x1e3ce508, v80
	v_mul_f32_e32 v81, 0x42fe0000, v81
	v_div_scale_f32 v82, s[4:5], v80, v80, v81
	v_rcp_f32_e32 v83, v82
	s_lshl_b64 s[4:5], s[2:3], 11
	v_fma_f32 v84, -v82, v83, 1.0
	v_fmac_f32_e32 v83, v84, v83
	v_div_scale_f32 v84, vcc, v81, v80, v81
	v_mul_f32_e32 v85, v84, v83
	v_fma_f32 v86, -v82, v85, v84
	v_fmac_f32_e32 v85, v86, v83
	v_fma_f32 v82, -v82, v85, v84
	v_div_fmas_f32 v82, v82, v83, v85
	v_div_fixup_f32 v82, v82, v80, v81
	v_lshl_add_u64 v[84:85], v[66:67], 0, s[18:19]
	v_pk_mul_f32 v[90:91], v[44:45], v[82:83] op_sel_hi:[1,0]
	global_store_dwordx2 v[84:85], v[88:89], off nt
	v_pk_mul_f32 v[88:89], v[46:47], v[82:83] op_sel_hi:[1,0]
	v_rndne_f32_e32 v83, v91
	v_rndne_f32_e32 v81, v90
	v_cvt_i32_f32_e32 v83, v83
	v_rndne_f32_e32 v88, v88
	v_rndne_f32_e32 v89, v89
	v_cvt_i32_f32_e32 v81, v81
	v_cvt_i32_f32_sdwa v88, v88 dst_sel:WORD_1 dst_unused:UNUSED_PAD src0_sel:DWORD
	v_cvt_i32_f32_e32 v89, v89
	v_lshlrev_b32_e32 v83, 8, v83
	v_and_b32_e32 v83, 0xff00, v83
	v_and_b32_e32 v88, 0xff0000, v88
	v_perm_b32 v81, v89, v81, s16
	v_lshl_add_u64 v[86:87], v[68:69], 0, s[4:5]
	v_or3_b32 v81, v81, v83, v88
	global_store_dword v[86:87], v81, off nt
	v_cvt_pk_bf16_f32 v88, v40, v41
	v_cvt_pk_bf16_f32 v89, v42, v43
	v_pk_mul_f32 v[90:91], v[40:41], v[82:83] op_sel_hi:[1,0]
	global_store_dwordx2 v[84:85], v[88:89], off offset:512 nt
	v_pk_mul_f32 v[88:89], v[42:43], v[82:83] op_sel_hi:[1,0]
	v_rndne_f32_e32 v83, v91
	v_rndne_f32_e32 v81, v90
	v_cvt_i32_f32_e32 v83, v83
	v_rndne_f32_e32 v88, v88
	v_rndne_f32_e32 v89, v89
	v_cvt_i32_f32_e32 v81, v81
	v_cvt_i32_f32_sdwa v88, v88 dst_sel:WORD_1 dst_unused:UNUSED_PAD src0_sel:DWORD
	v_cvt_i32_f32_e32 v89, v89
	v_lshlrev_b32_e32 v83, 8, v83
	v_and_b32_e32 v83, 0xff00, v83
	v_and_b32_e32 v88, 0xff0000, v88
	v_perm_b32 v81, v89, v81, s16
	v_or3_b32 v81, v81, v83, v88
	global_store_dword v[86:87], v81, off offset:256 nt
	v_cvt_pk_bf16_f32 v88, v36, v37
	v_cvt_pk_bf16_f32 v89, v38, v39
	v_pk_mul_f32 v[90:91], v[36:37], v[82:83] op_sel_hi:[1,0]
	global_store_dwordx2 v[84:85], v[88:89], off offset:1024 nt
	v_pk_mul_f32 v[88:89], v[38:39], v[82:83] op_sel_hi:[1,0]
	v_rndne_f32_e32 v83, v91
	v_rndne_f32_e32 v81, v90
	v_cvt_i32_f32_e32 v83, v83
	v_rndne_f32_e32 v88, v88
	v_rndne_f32_e32 v89, v89
	v_cvt_i32_f32_e32 v81, v81
	v_cvt_i32_f32_sdwa v88, v88 dst_sel:WORD_1 dst_unused:UNUSED_PAD src0_sel:DWORD
	v_cvt_i32_f32_e32 v89, v89
	v_lshlrev_b32_e32 v83, 8, v83
	v_and_b32_e32 v83, 0xff00, v83
	v_and_b32_e32 v88, 0xff0000, v88
	v_perm_b32 v81, v89, v81, s16
	v_or3_b32 v81, v81, v83, v88
	global_store_dword v[86:87], v81, off offset:512 nt
	v_cvt_pk_bf16_f32 v88, v32, v33
	v_cvt_pk_bf16_f32 v89, v34, v35
	v_pk_mul_f32 v[90:91], v[32:33], v[82:83] op_sel_hi:[1,0]
	global_store_dwordx2 v[84:85], v[88:89], off offset:1536 nt
	v_pk_mul_f32 v[88:89], v[34:35], v[82:83] op_sel_hi:[1,0]
	v_rndne_f32_e32 v83, v91
	v_rndne_f32_e32 v81, v90
	v_cvt_i32_f32_e32 v83, v83
	v_rndne_f32_e32 v88, v88
	v_rndne_f32_e32 v89, v89
	v_cvt_i32_f32_e32 v81, v81
	v_cvt_i32_f32_sdwa v88, v88 dst_sel:WORD_1 dst_unused:UNUSED_PAD src0_sel:DWORD
	v_cvt_i32_f32_e32 v89, v89
	v_lshlrev_b32_e32 v83, 8, v83
	v_and_b32_e32 v83, 0xff00, v83
	v_and_b32_e32 v88, 0xff0000, v88
	v_perm_b32 v81, v89, v81, s16
	v_or3_b32 v81, v81, v83, v88
	global_store_dword v[86:87], v81, off offset:768 nt
	v_cvt_pk_bf16_f32 v88, v60, v61
	v_cvt_pk_bf16_f32 v89, v62, v63
	v_pk_mul_f32 v[90:91], v[60:61], v[82:83] op_sel_hi:[1,0]
	global_store_dwordx2 v[84:85], v[88:89], off offset:2048 nt
	v_pk_mul_f32 v[88:89], v[62:63], v[82:83] op_sel_hi:[1,0]
	v_rndne_f32_e32 v83, v91
	v_rndne_f32_e32 v81, v90
	v_cvt_i32_f32_e32 v83, v83
	v_rndne_f32_e32 v88, v88
	v_rndne_f32_e32 v89, v89
	v_cvt_i32_f32_e32 v81, v81
	v_cvt_i32_f32_sdwa v88, v88 dst_sel:WORD_1 dst_unused:UNUSED_PAD src0_sel:DWORD
	v_cvt_i32_f32_e32 v89, v89
	v_lshlrev_b32_e32 v83, 8, v83
	v_and_b32_e32 v83, 0xff00, v83
	v_and_b32_e32 v88, 0xff0000, v88
	v_perm_b32 v81, v89, v81, s16
	v_or3_b32 v81, v81, v83, v88
	global_store_dword v[86:87], v81, off offset:1024 nt
	v_cvt_pk_bf16_f32 v88, v56, v57
	v_cvt_pk_bf16_f32 v89, v58, v59
	v_pk_mul_f32 v[90:91], v[56:57], v[82:83] op_sel_hi:[1,0]
	global_store_dwordx2 v[84:85], v[88:89], off offset:2560 nt
	v_pk_mul_f32 v[88:89], v[58:59], v[82:83] op_sel_hi:[1,0]
	v_rndne_f32_e32 v83, v91
	v_rndne_f32_e32 v81, v90
	v_cvt_i32_f32_e32 v83, v83
	v_rndne_f32_e32 v88, v88
	v_rndne_f32_e32 v89, v89
	v_cvt_i32_f32_e32 v81, v81
	v_cvt_i32_f32_sdwa v88, v88 dst_sel:WORD_1 dst_unused:UNUSED_PAD src0_sel:DWORD
	v_cvt_i32_f32_e32 v89, v89
	v_lshlrev_b32_e32 v83, 8, v83
	v_and_b32_e32 v83, 0xff00, v83
	v_and_b32_e32 v88, 0xff0000, v88
	v_perm_b32 v81, v89, v81, s16
	v_or3_b32 v81, v81, v83, v88
	global_store_dword v[86:87], v81, off offset:1280 nt
	v_cvt_pk_bf16_f32 v88, v52, v53
	v_cvt_pk_bf16_f32 v89, v54, v55
	v_pk_mul_f32 v[90:91], v[52:53], v[82:83] op_sel_hi:[1,0]
	global_store_dwordx2 v[84:85], v[88:89], off offset:3072 nt
	v_pk_mul_f32 v[88:89], v[54:55], v[82:83] op_sel_hi:[1,0]
	v_rndne_f32_e32 v83, v91
	v_rndne_f32_e32 v81, v90
	v_cvt_i32_f32_e32 v83, v83
	v_rndne_f32_e32 v88, v88
	v_rndne_f32_e32 v89, v89
	v_cvt_i32_f32_e32 v81, v81
	v_cvt_i32_f32_sdwa v88, v88 dst_sel:WORD_1 dst_unused:UNUSED_PAD src0_sel:DWORD
	v_cvt_i32_f32_e32 v89, v89
	v_lshlrev_b32_e32 v83, 8, v83
	v_and_b32_e32 v83, 0xff00, v83
	v_and_b32_e32 v88, 0xff0000, v88
	v_perm_b32 v81, v89, v81, s16
	v_or3_b32 v81, v81, v83, v88
	global_store_dword v[86:87], v81, off offset:1536 nt
	v_cvt_pk_bf16_f32 v88, v48, v49
	v_cvt_pk_bf16_f32 v89, v50, v51
	global_store_dwordx2 v[84:85], v[88:89], off offset:3584 nt
	v_pk_mul_f32 v[84:85], v[50:51], v[82:83] op_sel_hi:[1,0]
	v_pk_mul_f32 v[82:83], v[48:49], v[82:83] op_sel_hi:[1,0]
	s_nop 0
	v_rndne_f32_e32 v81, v82
	v_rndne_f32_e32 v82, v83
	v_cvt_i32_f32_e32 v82, v82
	v_rndne_f32_e32 v83, v84
	v_rndne_f32_e32 v84, v85
	v_cvt_i32_f32_e32 v81, v81
	v_cvt_i32_f32_sdwa v83, v83 dst_sel:WORD_1 dst_unused:UNUSED_PAD src0_sel:DWORD
	v_cvt_i32_f32_e32 v84, v84
	v_lshlrev_b32_e32 v82, 8, v82
	v_and_b32_e32 v82, 0xff00, v82
	v_and_b32_e32 v83, 0xff0000, v83
	v_perm_b32 v81, v84, v81, s16
	v_or3_b32 v81, v81, v82, v83
	global_store_dword v[86:87], v81, off offset:1792 nt
	s_and_saveexec_b64 s[4:5], s[0:1]
	s_cbranch_execz .LBB0_150
	s_lshl_b64 s[18:19], s[2:3], 2
	s_add_u32 s18, s11, s18
	s_addc_u32 s19, s14, s19
	v_mul_f32_e32 v80, 0x3c010204, v80
	global_store_dword v65, v80, s[18:19] nt
	s_branch .LBB0_150

.LBB0_1865:
	s_waitcnt vmcnt(22)
	v_lshlrev_b32_e32 v124, 16, v4
	v_and_b32_e32 v125, 0xffff0000, v4
	v_lshlrev_b32_e32 v126, 16, v5
	v_and_b32_e32 v127, 0xffff0000, v5
	s_waitcnt vmcnt(21)
	v_lshlrev_b32_e32 v128, 16, v6
	v_and_b32_e32 v129, 0xffff0000, v6
	v_lshlrev_b32_e32 v130, 16, v7
	v_and_b32_e32 v131, 0xffff0000, v7
	v_lshlrev_b32_e32 v120, 16, v2
	v_and_b32_e32 v121, 0xffff0000, v2
	v_lshlrev_b32_e32 v122, 16, v3
	v_and_b32_e32 v123, 0xffff0000, v3
	v_pk_add_f32 v[128:129], v[128:129], v[124:125]
	v_pk_add_f32 v[124:125], v[130:131], v[126:127]
	v_pk_add_f32 v[126:127], v[128:129], v[120:121]
	v_pk_add_f32 v[124:125], v[124:125], v[122:123]
	v_mul_f32_e32 v120, v127, v127
	v_mul_f32_e32 v121, v125, v125
	v_fmac_f32_e32 v120, v126, v126
	v_fmac_f32_e32 v121, v124, v124
	s_waitcnt vmcnt(19)
	v_lshlrev_b32_e32 v128, 16, v10
	v_and_b32_e32 v129, 0xffff0000, v10
	v_lshlrev_b32_e32 v130, 16, v11
	v_and_b32_e32 v131, 0xffff0000, v11
	s_waitcnt vmcnt(18)
	v_lshlrev_b32_e32 v132, 16, v12
	v_and_b32_e32 v133, 0xffff0000, v12
	v_lshlrev_b32_e32 v134, 16, v13
	v_and_b32_e32 v135, 0xffff0000, v13
	v_add_f32_e32 v136, v120, v121
	v_lshlrev_b32_e32 v122, 16, v8
	v_and_b32_e32 v123, 0xffff0000, v8
	v_lshlrev_b32_e32 v120, 16, v9
	v_and_b32_e32 v121, 0xffff0000, v9
	v_pk_add_f32 v[128:129], v[132:133], v[128:129]
	v_pk_add_f32 v[130:131], v[134:135], v[130:131]
	v_pk_add_f32 v[122:123], v[128:129], v[122:123]
	v_pk_add_f32 v[120:121], v[130:131], v[120:121]
	v_mul_f32_e32 v128, v123, v123
	v_mul_f32_e32 v129, v121, v121
	v_fmac_f32_e32 v128, v122, v122
	v_fmac_f32_e32 v129, v120, v120
	v_add_f32_e32 v128, v128, v129
	v_add_f32_e32 v140, v136, v128
	s_waitcnt vmcnt(16)
	v_lshlrev_b32_e32 v132, 16, v16
	v_and_b32_e32 v133, 0xffff0000, v16
	v_lshlrev_b32_e32 v134, 16, v17
	v_and_b32_e32 v135, 0xffff0000, v17
	s_waitcnt vmcnt(15)
	v_lshlrev_b32_e32 v136, 16, v18
	v_and_b32_e32 v137, 0xffff0000, v18
	v_lshlrev_b32_e32 v138, 16, v19
	v_and_b32_e32 v139, 0xffff0000, v19
	v_lshlrev_b32_e32 v130, 16, v14
	v_and_b32_e32 v131, 0xffff0000, v14
	v_lshlrev_b32_e32 v128, 16, v15
	v_and_b32_e32 v129, 0xffff0000, v15
	v_pk_add_f32 v[132:133], v[136:137], v[132:133]
	v_pk_add_f32 v[134:135], v[138:139], v[134:135]
	v_pk_add_f32 v[130:131], v[132:133], v[130:131]
	v_pk_add_f32 v[128:129], v[134:135], v[128:129]
	v_mul_f32_e32 v132, v131, v131
	v_mul_f32_e32 v133, v129, v129
	v_fmac_f32_e32 v132, v130, v130
	v_fmac_f32_e32 v133, v128, v128
	v_add_f32_e32 v132, v132, v133
	v_add_f32_e32 v144, v132, v140
	s_waitcnt vmcnt(13)
	v_lshlrev_b32_e32 v136, 16, v22
	v_and_b32_e32 v137, 0xffff0000, v22
	v_lshlrev_b32_e32 v138, 16, v23
	v_and_b32_e32 v139, 0xffff0000, v23
	s_waitcnt vmcnt(12)
	v_lshlrev_b32_e32 v140, 16, v24
	v_and_b32_e32 v141, 0xffff0000, v24
	v_lshlrev_b32_e32 v142, 16, v25
	v_and_b32_e32 v143, 0xffff0000, v25
	v_lshlrev_b32_e32 v134, 16, v20
	v_and_b32_e32 v135, 0xffff0000, v20
	v_lshlrev_b32_e32 v132, 16, v21
	v_and_b32_e32 v133, 0xffff0000, v21
	v_pk_add_f32 v[136:137], v[140:141], v[136:137]
	v_pk_add_f32 v[138:139], v[142:143], v[138:139]
	v_pk_add_f32 v[134:135], v[136:137], v[134:135]
	v_pk_add_f32 v[132:133], v[138:139], v[132:133]
	v_mul_f32_e32 v136, v135, v135
	v_mul_f32_e32 v137, v133, v133
	v_fmac_f32_e32 v136, v134, v134
	v_fmac_f32_e32 v137, v132, v132
	v_add_f32_e32 v136, v136, v137
	v_add_f32_e32 v148, v136, v144
	s_waitcnt vmcnt(10)
	v_lshlrev_b32_e32 v140, 16, v30
	v_and_b32_e32 v141, 0xffff0000, v30
	v_lshlrev_b32_e32 v142, 16, v31
	v_and_b32_e32 v143, 0xffff0000, v31
	s_waitcnt vmcnt(9)
	v_lshlrev_b32_e32 v144, 16, v34
	v_and_b32_e32 v145, 0xffff0000, v34
	v_lshlrev_b32_e32 v146, 16, v35
	v_and_b32_e32 v147, 0xffff0000, v35
	v_lshlrev_b32_e32 v138, 16, v28
	v_and_b32_e32 v139, 0xffff0000, v28
	v_lshlrev_b32_e32 v136, 16, v29
	v_and_b32_e32 v137, 0xffff0000, v29
	v_pk_add_f32 v[140:141], v[144:145], v[140:141]
	v_pk_add_f32 v[142:143], v[146:147], v[142:143]
	v_pk_add_f32 v[138:139], v[140:141], v[138:139]
	v_pk_add_f32 v[136:137], v[142:143], v[136:137]
	v_mul_f32_e32 v140, v139, v139
	v_mul_f32_e32 v141, v137, v137
	v_fmac_f32_e32 v140, v138, v138
	v_fmac_f32_e32 v141, v136, v136
	v_add_f32_e32 v140, v140, v141
	v_add_f32_e32 v152, v140, v148
	s_waitcnt vmcnt(7)
	v_lshlrev_b32_e32 v144, 16, v54
	v_and_b32_e32 v145, 0xffff0000, v54
	v_lshlrev_b32_e32 v146, 16, v55
	v_and_b32_e32 v147, 0xffff0000, v55
	s_waitcnt vmcnt(6)
	v_lshlrev_b32_e32 v148, 16, v56
	v_and_b32_e32 v149, 0xffff0000, v56
	v_lshlrev_b32_e32 v150, 16, v57
	v_and_b32_e32 v151, 0xffff0000, v57
	v_lshlrev_b32_e32 v142, 16, v36
	v_and_b32_e32 v143, 0xffff0000, v36
	v_lshlrev_b32_e32 v140, 16, v37
	v_and_b32_e32 v141, 0xffff0000, v37
	v_pk_add_f32 v[144:145], v[148:149], v[144:145]
	v_pk_add_f32 v[146:147], v[150:151], v[146:147]
	v_pk_add_f32 v[142:143], v[144:145], v[142:143]
	v_pk_add_f32 v[140:141], v[146:147], v[140:141]
	v_mul_f32_e32 v144, v143, v143
	v_mul_f32_e32 v145, v141, v141
	v_fmac_f32_e32 v144, v142, v142
	v_fmac_f32_e32 v145, v140, v140
	v_add_f32_e32 v144, v144, v145
	s_waitcnt vmcnt(4)
	v_lshlrev_b32_e32 v148, 16, v62
	v_and_b32_e32 v149, 0xffff0000, v62
	v_lshlrev_b32_e32 v150, 16, v63
	v_and_b32_e32 v151, 0xffff0000, v63
	s_waitcnt vmcnt(3)
	v_lshlrev_b32_e32 v154, 16, v64
	v_and_b32_e32 v155, 0xffff0000, v64
	v_lshlrev_b32_e32 v156, 16, v65
	v_and_b32_e32 v157, 0xffff0000, v65
	v_add_f32_e32 v152, v144, v152
	v_lshlrev_b32_e32 v146, 16, v60
	v_and_b32_e32 v147, 0xffff0000, v60
	v_lshlrev_b32_e32 v144, 16, v61
	v_and_b32_e32 v145, 0xffff0000, v61
	v_pk_add_f32 v[148:149], v[154:155], v[148:149]
	v_pk_add_f32 v[150:151], v[156:157], v[150:151]
	v_pk_add_f32 v[146:147], v[148:149], v[146:147]
	v_pk_add_f32 v[144:145], v[150:151], v[144:145]
	v_mul_f32_e32 v148, v147, v147
	v_mul_f32_e32 v149, v145, v145
	v_fmac_f32_e32 v148, v146, v146
	v_fmac_f32_e32 v149, v144, v144
	v_add_f32_e32 v148, v148, v149
	s_waitcnt vmcnt(1)
	v_lshlrev_b32_e32 v154, 16, v68
	v_and_b32_e32 v155, 0xffff0000, v68
	v_lshlrev_b32_e32 v156, 16, v69
	v_and_b32_e32 v157, 0xffff0000, v69
	s_waitcnt vmcnt(0)
	v_lshlrev_b32_e32 v158, 16, v70
	v_and_b32_e32 v159, 0xffff0000, v70
	v_lshlrev_b32_e32 v160, 16, v71
	v_and_b32_e32 v161, 0xffff0000, v71
	v_add_f32_e32 v152, v148, v152
	v_lshlrev_b32_e32 v150, 16, v66
	v_and_b32_e32 v151, 0xffff0000, v66
	v_lshlrev_b32_e32 v148, 16, v67
	v_and_b32_e32 v149, 0xffff0000, v67
	v_pk_add_f32 v[154:155], v[158:159], v[154:155]
	v_pk_add_f32 v[156:157], v[160:161], v[156:157]
	v_pk_add_f32 v[150:151], v[154:155], v[150:151]
	v_pk_add_f32 v[148:149], v[156:157], v[148:149]
	v_mul_f32_e32 v154, v151, v151
	v_mul_f32_e32 v155, v149, v149
	v_fmac_f32_e32 v154, v150, v150
	v_fmac_f32_e32 v155, v148, v148
	v_add_f32_e32 v154, v154, v155
	v_add_f32_e32 v152, v154, v152
	ds_bpermute_b32 v154, v1, v152
	v_readlane_b32 s16, v253, 24
	v_readlane_b32 s17, v253, 25
	s_waitcnt lgkmcnt(0)
	v_add_f32_e32 v152, v152, v154
	ds_bpermute_b32 v154, v41, v152
	s_waitcnt lgkmcnt(0)
	v_add_f32_e32 v152, v152, v154
	ds_bpermute_b32 v154, v45, v152
	s_waitcnt lgkmcnt(0)
	v_add_f32_e32 v152, v152, v154
	ds_bpermute_b32 v154, v49, v152
	s_waitcnt lgkmcnt(0)
	v_add_f32_e32 v152, v152, v154
	ds_bpermute_b32 v154, v53, v152
	s_waitcnt lgkmcnt(0)
	v_add_f32_e32 v152, v152, v154
	ds_bpermute_b32 v154, v153, v152
	s_waitcnt lgkmcnt(0)
	v_add_f32_e32 v152, v152, v154
	v_fmamk_f32 v152, v152, 0x3a000000, v189
	v_mul_f32_e32 v154, 0x4f800000, v152
	v_cmp_gt_f32_e32 vcc, s84, v152
	s_nop 1
	v_cndmask_b32_e32 v152, v152, v154, vcc
	v_sqrt_f32_e32 v154, v152
	s_nop 0
	v_add_u32_e32 v155, -1, v154
	v_fma_f32 v156, -v155, v154, v152
	v_cmp_ge_f32_e64 s[36:37], 0, v156
	v_add_u32_e32 v156, 1, v154
	s_nop 0
	v_cndmask_b32_e64 v155, v154, v155, s[36:37]
	v_fma_f32 v154, -v156, v154, v152
	v_cmp_lt_f32_e64 s[36:37], 0, v154
	s_nop 1
	v_cndmask_b32_e64 v154, v155, v156, s[36:37]
	v_mul_f32_e32 v155, 0x37800000, v154
	v_cndmask_b32_e32 v154, v154, v155, vcc
	v_cmp_class_f32_e32 vcc, v152, v190
	s_nop 1
	v_cndmask_b32_e32 v152, v154, v152, vcc
	v_div_scale_f32 v154, s[12:13], v152, v152, 1.0
	v_rcp_f32_e32 v155, v154
	s_mov_b64 s[12:13], -1
	v_fma_f32 v156, -v154, v155, 1.0
	v_fmac_f32_e32 v155, v156, v155
	v_div_scale_f32 v156, vcc, 1.0, v152, 1.0
	v_mul_f32_e32 v157, v156, v155
	v_fma_f32 v158, -v154, v157, v156
	v_fmac_f32_e32 v157, v158, v155
	v_fma_f32 v154, -v154, v157, v156
	v_div_fmas_f32 v154, v154, v155, v157
	v_div_fixup_f32 v152, v154, v152, 1.0
	s_and_b64 vcc, exec, s[16:17]
	s_cbranch_vccz .LBB0_1869
	v_max_f32_e64 v154, |v125|, |v125|
	v_max_f32_e64 v155, |v124|, |v124|
	v_max_f32_e32 v154, v155, v154
	v_max_f32_e64 v155, |v121|, |v121|
	v_max_f32_e64 v156, |v120|, |v120|
	v_max_f32_e32 v155, v156, v155
	v_max3_f32 v154, |v126|, |v127|, v154
	v_max3_f32 v155, |v122|, |v123|, v155
	v_max3_f32 v154, v154, 0, v155
	v_max_f32_e64 v155, |v129|, |v129|
	v_max_f32_e64 v156, |v128|, |v128|
	v_max_f32_e32 v155, v156, v155
	v_max_f32_e64 v156, |v133|, |v133|
	v_max_f32_e64 v157, |v132|, |v132|
	v_max_f32_e32 v156, v157, v156
	v_max3_f32 v155, |v130|, |v131|, v155
	v_max3_f32 v156, |v134|, |v135|, v156
	v_max3_f32 v154, v154, v155, v156
	v_max_f32_e64 v155, |v137|, |v137|
	v_max_f32_e64 v156, |v136|, |v136|
	v_max_f32_e32 v155, v156, v155
	v_max_f32_e64 v156, |v141|, |v141|
	v_max_f32_e64 v157, |v140|, |v140|
	v_max_f32_e32 v156, v157, v156
	v_max3_f32 v155, |v138|, |v139|, v155
	v_max3_f32 v156, |v142|, |v143|, v156
	v_max3_f32 v154, v154, v155, v156
	v_max_f32_e64 v155, |v145|, |v145|
	v_max_f32_e64 v156, |v144|, |v144|
	v_max_f32_e32 v155, v156, v155
	v_max_f32_e64 v156, |v149|, |v149|
	v_max_f32_e64 v157, |v148|, |v148|
	v_max_f32_e32 v156, v157, v156
	v_max3_f32 v155, |v146|, |v147|, v155
	v_max3_f32 v156, |v150|, |v151|, v156
	v_max3_f32 v154, v154, v155, v156
	ds_bpermute_b32 v155, v1, v154
	s_ashr_i32 s9, s8, 31
	s_waitcnt lgkmcnt(0)
	v_max_f32_e32 v155, v155, v155
	v_max_f32_e32 v154, v154, v155
	ds_bpermute_b32 v155, v41, v154
	s_waitcnt lgkmcnt(0)
	v_max_f32_e32 v155, v155, v155
	v_max_f32_e32 v154, v154, v155
	ds_bpermute_b32 v155, v45, v154
	s_waitcnt lgkmcnt(0)
	v_max_f32_e32 v155, v155, v155
	v_max_f32_e32 v154, v154, v155
	ds_bpermute_b32 v155, v49, v154
	s_waitcnt lgkmcnt(0)
	v_max_f32_e32 v155, v155, v155
	v_max_f32_e32 v154, v154, v155
	ds_bpermute_b32 v155, v53, v154
	s_waitcnt lgkmcnt(0)
	v_max_f32_e32 v155, v155, v155
	v_max_f32_e32 v154, v154, v155
	ds_bpermute_b32 v155, v153, v154
	s_waitcnt lgkmcnt(0)
	v_max_f32_e32 v155, v155, v155
	v_max_f32_e32 v154, v154, v155
	v_mul_f32_e32 v154, v152, v154
	v_max_f32_e32 v154, 0x1e3ce508, v154
	s_and_saveexec_b64 s[12:13], s[34:35]
	s_cbranch_execz .LBB0_1868
	s_lshl_b64 s[16:17], s[8:9], 2
	v_readlane_b32 s18, v253, 26
	v_readlane_b32 s19, v253, 27
	s_add_u32 s16, s18, s16
	s_addc_u32 s17, s19, s17
	v_mul_f32_e32 v155, 0x3c010204, v154
	global_store_dword v173, v155, s[16:17] nt
.LBB0_1868:
	s_or_b64 exec, exec, s[12:13]
	v_mul_f32_e32 v155, 0x42fe0000, v152
	v_div_scale_f32 v156, s[12:13], v154, v154, v155
	v_rcp_f32_e32 v157, v156
	v_div_scale_f32 v158, vcc, v155, v154, v155
	s_lshl_b64 s[12:13], s[8:9], 11
	v_fma_f32 v159, -v156, v157, 1.0
	v_fmac_f32_e32 v157, v159, v157
	v_mul_f32_e32 v159, v158, v157
	v_fma_f32 v160, -v156, v159, v158
	v_fmac_f32_e32 v159, v160, v157
	v_fma_f32 v156, -v156, v159, v158
	v_div_fmas_f32 v156, v156, v157, v159
	v_div_fixup_f32 v154, v156, v154, v155
	v_lshl_add_u64 v[156:157], v[26:27], 0, s[12:13]
	s_lshl_b64 s[12:13], s[8:9], 12
	v_cvt_pk_bf16_f32 v158, v126, v127
	v_cvt_pk_bf16_f32 v159, v124, v125
	v_lshl_add_u64 v[160:161], v[32:33], 0, s[12:13]
	v_pk_mul_f32 v[162:163], v[126:127], v[154:155] op_sel_hi:[1,0]
	global_store_dwordx2 v[160:161], v[158:159], off nt
	v_pk_mul_f32 v[158:159], v[124:125], v[154:155] op_sel_hi:[1,0]
	v_rndne_f32_e32 v155, v162
	v_rndne_f32_e32 v162, v163
	v_cvt_i32_f32_e32 v162, v162
	v_rndne_f32_e32 v158, v158
	v_rndne_f32_e32 v159, v159
	v_cvt_i32_f32_e32 v155, v155
	v_cvt_i32_f32_sdwa v158, v158 dst_sel:WORD_1 dst_unused:UNUSED_PAD src0_sel:DWORD
	v_cvt_i32_f32_e32 v159, v159
	v_lshlrev_b32_e32 v162, 8, v162
	v_and_b32_e32 v162, 0xff00, v162
	v_and_b32_e32 v158, 0xff0000, v158
	v_perm_b32 v155, v159, v155, s89
	v_or3_b32 v155, v155, v162, v158
	global_store_dword v[156:157], v155, off nt
	v_cvt_pk_bf16_f32 v158, v122, v123
	v_cvt_pk_bf16_f32 v159, v120, v121
	v_pk_mul_f32 v[162:163], v[122:123], v[154:155] op_sel_hi:[1,0]
	global_store_dwordx2 v[160:161], v[158:159], off offset:512 nt
	v_pk_mul_f32 v[158:159], v[120:121], v[154:155] op_sel_hi:[1,0]
	v_rndne_f32_e32 v155, v162
	v_rndne_f32_e32 v162, v163
	v_cvt_i32_f32_e32 v162, v162
	v_rndne_f32_e32 v158, v158
	v_rndne_f32_e32 v159, v159
	v_cvt_i32_f32_e32 v155, v155
	v_cvt_i32_f32_sdwa v158, v158 dst_sel:WORD_1 dst_unused:UNUSED_PAD src0_sel:DWORD
	v_cvt_i32_f32_e32 v159, v159
	v_lshlrev_b32_e32 v162, 8, v162
	v_and_b32_e32 v162, 0xff00, v162
	v_and_b32_e32 v158, 0xff0000, v158
	v_perm_b32 v155, v159, v155, s89
	v_or3_b32 v155, v155, v162, v158
	global_store_dword v[156:157], v155, off offset:256 nt
	v_cvt_pk_bf16_f32 v158, v130, v131
	v_cvt_pk_bf16_f32 v159, v128, v129
	v_pk_mul_f32 v[162:163], v[130:131], v[154:155] op_sel_hi:[1,0]
	global_store_dwordx2 v[160:161], v[158:159], off offset:1024 nt
	v_pk_mul_f32 v[158:159], v[128:129], v[154:155] op_sel_hi:[1,0]
	v_rndne_f32_e32 v155, v162
	v_rndne_f32_e32 v162, v163
	v_cvt_i32_f32_e32 v162, v162
	v_rndne_f32_e32 v158, v158
	v_rndne_f32_e32 v159, v159
	v_cvt_i32_f32_e32 v155, v155
	v_cvt_i32_f32_sdwa v158, v158 dst_sel:WORD_1 dst_unused:UNUSED_PAD src0_sel:DWORD
	v_cvt_i32_f32_e32 v159, v159
	v_lshlrev_b32_e32 v162, 8, v162
	v_and_b32_e32 v162, 0xff00, v162
	v_and_b32_e32 v158, 0xff0000, v158
	v_perm_b32 v155, v159, v155, s89
	v_or3_b32 v155, v155, v162, v158
	global_store_dword v[156:157], v155, off offset:512 nt
	v_cvt_pk_bf16_f32 v158, v134, v135
	v_cvt_pk_bf16_f32 v159, v132, v133
	v_pk_mul_f32 v[162:163], v[134:135], v[154:155] op_sel_hi:[1,0]
	global_store_dwordx2 v[160:161], v[158:159], off offset:1536 nt
	v_pk_mul_f32 v[158:159], v[132:133], v[154:155] op_sel_hi:[1,0]
	v_rndne_f32_e32 v155, v162
	v_rndne_f32_e32 v162, v163
	v_cvt_i32_f32_e32 v162, v162
	v_rndne_f32_e32 v158, v158
	v_rndne_f32_e32 v159, v159
	v_cvt_i32_f32_e32 v155, v155
	v_cvt_i32_f32_sdwa v158, v158 dst_sel:WORD_1 dst_unused:UNUSED_PAD src0_sel:DWORD
	v_cvt_i32_f32_e32 v159, v159
	v_lshlrev_b32_e32 v162, 8, v162
	v_and_b32_e32 v162, 0xff00, v162
	v_and_b32_e32 v158, 0xff0000, v158
	v_perm_b32 v155, v159, v155, s89
	v_or3_b32 v155, v155, v162, v158
	global_store_dword v[156:157], v155, off offset:768 nt
	v_cvt_pk_bf16_f32 v158, v138, v139
	v_cvt_pk_bf16_f32 v159, v136, v137
	v_pk_mul_f32 v[162:163], v[138:139], v[154:155] op_sel_hi:[1,0]
	global_store_dwordx2 v[160:161], v[158:159], off offset:2048 nt
	v_pk_mul_f32 v[158:159], v[136:137], v[154:155] op_sel_hi:[1,0]
	v_rndne_f32_e32 v155, v162
	v_rndne_f32_e32 v162, v163
	v_cvt_i32_f32_e32 v162, v162
	v_rndne_f32_e32 v158, v158
	v_rndne_f32_e32 v159, v159
	v_cvt_i32_f32_e32 v155, v155
	v_cvt_i32_f32_sdwa v158, v158 dst_sel:WORD_1 dst_unused:UNUSED_PAD src0_sel:DWORD
	v_cvt_i32_f32_e32 v159, v159
	v_lshlrev_b32_e32 v162, 8, v162
	v_and_b32_e32 v162, 0xff00, v162
	v_and_b32_e32 v158, 0xff0000, v158
	v_perm_b32 v155, v159, v155, s89
	v_or3_b32 v155, v155, v162, v158
	global_store_dword v[156:157], v155, off offset:1024 nt
	v_cvt_pk_bf16_f32 v158, v142, v143
	v_cvt_pk_bf16_f32 v159, v140, v141
	v_pk_mul_f32 v[162:163], v[142:143], v[154:155] op_sel_hi:[1,0]
	global_store_dwordx2 v[160:161], v[158:159], off offset:2560 nt
	v_pk_mul_f32 v[158:159], v[140:141], v[154:155] op_sel_hi:[1,0]
	v_rndne_f32_e32 v155, v162
	v_rndne_f32_e32 v162, v163
	v_cvt_i32_f32_e32 v162, v162
	v_rndne_f32_e32 v158, v158
	v_rndne_f32_e32 v159, v159
	v_cvt_i32_f32_e32 v155, v155
	v_cvt_i32_f32_sdwa v158, v158 dst_sel:WORD_1 dst_unused:UNUSED_PAD src0_sel:DWORD
	v_cvt_i32_f32_e32 v159, v159
	v_lshlrev_b32_e32 v162, 8, v162
	v_and_b32_e32 v162, 0xff00, v162
	v_and_b32_e32 v158, 0xff0000, v158
	v_perm_b32 v155, v159, v155, s89
	v_or3_b32 v155, v155, v162, v158
	global_store_dword v[156:157], v155, off offset:1280 nt
	v_cvt_pk_bf16_f32 v158, v146, v147
	v_cvt_pk_bf16_f32 v159, v144, v145
	v_pk_mul_f32 v[162:163], v[146:147], v[154:155] op_sel_hi:[1,0]
	global_store_dwordx2 v[160:161], v[158:159], off offset:3072 nt
	v_pk_mul_f32 v[158:159], v[144:145], v[154:155] op_sel_hi:[1,0]
	v_rndne_f32_e32 v155, v162
	v_rndne_f32_e32 v162, v163
	v_cvt_i32_f32_e32 v162, v162
	v_rndne_f32_e32 v158, v158
	v_rndne_f32_e32 v159, v159
	v_cvt_i32_f32_e32 v155, v155
	v_cvt_i32_f32_sdwa v158, v158 dst_sel:WORD_1 dst_unused:UNUSED_PAD src0_sel:DWORD
	v_cvt_i32_f32_e32 v159, v159
	v_lshlrev_b32_e32 v162, 8, v162
	v_and_b32_e32 v162, 0xff00, v162
	v_and_b32_e32 v158, 0xff0000, v158
	v_perm_b32 v155, v159, v155, s89
	v_or3_b32 v155, v155, v162, v158
	global_store_dword v[156:157], v155, off offset:1536 nt
	v_cvt_pk_bf16_f32 v158, v150, v151
	v_cvt_pk_bf16_f32 v159, v148, v149
	global_store_dwordx2 v[160:161], v[158:159], off offset:3584 nt
	v_pk_mul_f32 v[158:159], v[148:149], v[154:155] op_sel_hi:[1,0]
	v_pk_mul_f32 v[154:155], v[150:151], v[154:155] op_sel_hi:[1,0]
	v_rndne_f32_e32 v158, v158
	v_rndne_f32_e32 v155, v155
	v_rndne_f32_e32 v154, v154
	v_cvt_i32_f32_e32 v155, v155
	v_rndne_f32_e32 v159, v159
	v_cvt_i32_f32_e32 v154, v154
	v_cvt_i32_f32_sdwa v158, v158 dst_sel:WORD_1 dst_unused:UNUSED_PAD src0_sel:DWORD
	v_cvt_i32_f32_e32 v159, v159
	v_lshlrev_b32_e32 v155, 8, v155
	v_and_b32_e32 v155, 0xff00, v155
	v_and_b32_e32 v158, 0xff0000, v158
	v_perm_b32 v154, v159, v154, s89
	v_or3_b32 v154, v154, v155, v158
	s_mov_b64 s[12:13], 0
	global_store_dword v[156:157], v154, off offset:1792 nt
.LBB0_1869:
	s_and_b64 vcc, exec, s[12:13]
	s_cbranch_vccz .LBB0_1871
	global_load_dwordx4 v[208:211], v[38:39], off
	global_load_dwordx4 v[212:215], v[38:39], off offset:1024
	global_load_dwordx4 v[216:219], v[38:39], off offset:2048
	global_load_dwordx4 v[224:227], v[38:39], off offset:3072
	global_load_dwordx4 v[228:231], v[42:43], off
	global_load_dwordx4 v[232:235], v[46:47], off
	global_load_dwordx4 v[236:239], v[50:51], off
	global_load_dwordx4 v[240:243], v[58:59], off
	s_nop 0
	s_ashr_i32 s9, s8, 31
	v_readlane_b32 s36, v252, 24
	s_lshl_b64 s[12:13], s[8:9], 13
	v_readlane_b32 s48, v252, 36
	v_readlane_b32 s49, v252, 37
	s_add_u32 s12, s48, s12
	v_pk_mul_f32 v[124:125], v[124:125], v[152:153] op_sel_hi:[1,0]
	v_pk_mul_f32 v[158:159], v[126:127], v[152:153] op_sel_hi:[1,0]
	s_addc_u32 s13, s49, s13
	v_pk_mul_f32 v[120:121], v[120:121], v[152:153] op_sel_hi:[1,0]
	v_readlane_b32 s37, v252, 25
	v_readlane_b32 s38, v252, 26
	v_readlane_b32 s39, v252, 27
	v_readlane_b32 s40, v252, 28
	v_readlane_b32 s41, v252, 29
	v_readlane_b32 s42, v252, 30
	v_readlane_b32 s43, v252, 31
	v_readlane_b32 s44, v252, 32
	v_readlane_b32 s45, v252, 33
	v_readlane_b32 s46, v252, 34
	v_readlane_b32 s47, v252, 35
	v_readlane_b32 s50, v252, 38
	v_readlane_b32 s51, v252, 39
	s_waitcnt vmcnt(7)
	v_pk_mul_f32 v[126:127], v[124:125], v[210:211]
	v_pk_mul_f32 v[124:125], v[158:159], v[208:209]
	v_lshlrev_b32_e32 v156, 4, v0
	global_store_dwordx4 v156, v[124:127], s[12:13] nt
	s_nop 0
	v_pk_mul_f32 v[154:155], v[122:123], v[152:153] op_sel_hi:[1,0]
	s_waitcnt vmcnt(7)
	v_pk_mul_f32 v[122:123], v[120:121], v[214:215]
	v_pk_mul_f32 v[120:121], v[154:155], v[212:213]
	global_store_dwordx4 v156, v[120:123], s[12:13] offset:1024 nt
	s_nop 0
	v_pk_mul_f32 v[124:125], v[128:129], v[152:153] op_sel_hi:[1,0]
	v_pk_mul_f32 v[126:127], v[130:131], v[152:153] op_sel_hi:[1,0]
	s_waitcnt vmcnt(7)
	v_pk_mul_f32 v[122:123], v[124:125], v[218:219]
	v_pk_mul_f32 v[120:121], v[126:127], v[216:217]
	global_store_dwordx4 v156, v[120:123], s[12:13] offset:2048 nt
	s_nop 0
	v_pk_mul_f32 v[124:125], v[132:133], v[152:153] op_sel_hi:[1,0]
	v_pk_mul_f32 v[126:127], v[134:135], v[152:153] op_sel_hi:[1,0]
	s_waitcnt vmcnt(7)
	v_pk_mul_f32 v[122:123], v[124:125], v[226:227]
	v_pk_mul_f32 v[120:121], v[126:127], v[224:225]
	global_store_dwordx4 v156, v[120:123], s[12:13] offset:3072 nt
	s_nop 0
	v_pk_mul_f32 v[124:125], v[136:137], v[152:153] op_sel_hi:[1,0]
	v_pk_mul_f32 v[126:127], v[138:139], v[152:153] op_sel_hi:[1,0]
	s_waitcnt vmcnt(7)
	v_pk_mul_f32 v[122:123], v[124:125], v[230:231]
	v_pk_mul_f32 v[120:121], v[126:127], v[228:229]
	v_lshlrev_b32_e32 v124, 4, v40
	global_store_dwordx4 v124, v[120:123], s[12:13] nt
	s_nop 0
	v_pk_mul_f32 v[124:125], v[140:141], v[152:153] op_sel_hi:[1,0]
	v_pk_mul_f32 v[126:127], v[142:143], v[152:153] op_sel_hi:[1,0]
	s_waitcnt vmcnt(7)
	v_pk_mul_f32 v[122:123], v[124:125], v[234:235]
	v_pk_mul_f32 v[120:121], v[126:127], v[232:233]
	v_lshlrev_b32_e32 v124, 4, v44
	global_store_dwordx4 v124, v[120:123], s[12:13] nt
	s_nop 0
	v_pk_mul_f32 v[124:125], v[144:145], v[152:153] op_sel_hi:[1,0]
	v_pk_mul_f32 v[126:127], v[146:147], v[152:153] op_sel_hi:[1,0]
	s_waitcnt vmcnt(7)
	v_pk_mul_f32 v[122:123], v[124:125], v[238:239]
	v_pk_mul_f32 v[120:121], v[126:127], v[236:237]
	v_lshlrev_b32_e32 v124, 4, v48
	global_store_dwordx4 v124, v[120:123], s[12:13] nt
	s_nop 0
	v_pk_mul_f32 v[124:125], v[148:149], v[152:153] op_sel_hi:[1,0]
	v_pk_mul_f32 v[126:127], v[150:151], v[152:153] op_sel_hi:[1,0]
	s_waitcnt vmcnt(7)
	v_pk_mul_f32 v[122:123], v[124:125], v[242:243]
	v_pk_mul_f32 v[120:121], v[126:127], v[240:241]
	v_lshlrev_b32_e32 v124, 4, v52
	global_store_dwordx4 v124, v[120:123], s[12:13] nt

.LBB0_1874:
	v_lshlrev_b32_e32 v124, 16, v76
	v_and_b32_e32 v125, 0xffff0000, v76
	v_lshlrev_b32_e32 v126, 16, v77
	v_and_b32_e32 v127, 0xffff0000, v77
	v_lshlrev_b32_e32 v128, 16, v80
	v_and_b32_e32 v129, 0xffff0000, v80
	v_lshlrev_b32_e32 v130, 16, v81
	v_and_b32_e32 v131, 0xffff0000, v81
	v_lshlrev_b32_e32 v120, 16, v72
	v_and_b32_e32 v121, 0xffff0000, v72
	v_lshlrev_b32_e32 v122, 16, v73
	v_and_b32_e32 v123, 0xffff0000, v73
	v_pk_add_f32 v[128:129], v[124:125], v[128:129]
	v_pk_add_f32 v[124:125], v[126:127], v[130:131]
	v_pk_add_f32 v[126:127], v[128:129], v[120:121]
	v_pk_add_f32 v[124:125], v[124:125], v[122:123]
	v_mul_f32_e32 v120, v127, v127
	v_mul_f32_e32 v121, v125, v125
	v_fmac_f32_e32 v120, v126, v126
	v_fmac_f32_e32 v121, v124, v124
	v_lshlrev_b32_e32 v128, 16, v82
	v_and_b32_e32 v129, 0xffff0000, v82
	v_lshlrev_b32_e32 v130, 16, v83
	v_and_b32_e32 v131, 0xffff0000, v83
	v_lshlrev_b32_e32 v132, 16, v88
	v_and_b32_e32 v133, 0xffff0000, v88
	v_lshlrev_b32_e32 v134, 16, v89
	v_and_b32_e32 v135, 0xffff0000, v89
	v_add_f32_e32 v136, v120, v121
	v_lshlrev_b32_e32 v122, 16, v74
	v_and_b32_e32 v123, 0xffff0000, v74
	v_lshlrev_b32_e32 v120, 16, v75
	v_and_b32_e32 v121, 0xffff0000, v75
	v_pk_add_f32 v[128:129], v[128:129], v[132:133]
	v_pk_add_f32 v[130:131], v[130:131], v[134:135]
	v_pk_add_f32 v[122:123], v[128:129], v[122:123]
	v_pk_add_f32 v[120:121], v[130:131], v[120:121]
	v_mul_f32_e32 v128, v123, v123
	v_mul_f32_e32 v129, v121, v121
	v_fmac_f32_e32 v128, v122, v122
	v_fmac_f32_e32 v129, v120, v120
	v_add_f32_e32 v128, v128, v129
	v_add_f32_e32 v140, v128, v136
	v_lshlrev_b32_e32 v132, 16, v84
	v_and_b32_e32 v133, 0xffff0000, v84
	v_lshlrev_b32_e32 v134, 16, v85
	v_and_b32_e32 v135, 0xffff0000, v85
	v_lshlrev_b32_e32 v136, 16, v94
	v_and_b32_e32 v137, 0xffff0000, v94
	v_lshlrev_b32_e32 v138, 16, v95
	v_and_b32_e32 v139, 0xffff0000, v95
	v_lshlrev_b32_e32 v130, 16, v78
	v_and_b32_e32 v131, 0xffff0000, v78
	v_lshlrev_b32_e32 v128, 16, v79
	v_and_b32_e32 v129, 0xffff0000, v79
	v_pk_add_f32 v[132:133], v[132:133], v[136:137]
	v_pk_add_f32 v[134:135], v[134:135], v[138:139]
	v_pk_add_f32 v[130:131], v[132:133], v[130:131]
	v_pk_add_f32 v[128:129], v[134:135], v[128:129]
	v_mul_f32_e32 v132, v131, v131
	v_mul_f32_e32 v133, v129, v129
	v_fmac_f32_e32 v132, v130, v130
	v_fmac_f32_e32 v133, v128, v128
	v_add_f32_e32 v132, v132, v133
	v_add_f32_e32 v144, v132, v140
	v_lshlrev_b32_e32 v136, 16, v90
	v_and_b32_e32 v137, 0xffff0000, v90
	v_lshlrev_b32_e32 v138, 16, v91
	v_and_b32_e32 v139, 0xffff0000, v91
	v_lshlrev_b32_e32 v140, 16, v98
	v_and_b32_e32 v141, 0xffff0000, v98
	v_lshlrev_b32_e32 v142, 16, v99
	v_and_b32_e32 v143, 0xffff0000, v99
	v_lshlrev_b32_e32 v134, 16, v86
	v_and_b32_e32 v135, 0xffff0000, v86
	v_lshlrev_b32_e32 v132, 16, v87
	v_and_b32_e32 v133, 0xffff0000, v87
	v_pk_add_f32 v[136:137], v[136:137], v[140:141]
	v_pk_add_f32 v[138:139], v[138:139], v[142:143]
	v_pk_add_f32 v[134:135], v[136:137], v[134:135]
	v_pk_add_f32 v[132:133], v[138:139], v[132:133]
	v_mul_f32_e32 v136, v135, v135
	v_mul_f32_e32 v137, v133, v133
	v_fmac_f32_e32 v136, v134, v134
	v_fmac_f32_e32 v137, v132, v132
	v_add_f32_e32 v136, v136, v137
	v_add_f32_e32 v148, v136, v144
	v_lshlrev_b32_e32 v140, 16, v100
	v_and_b32_e32 v141, 0xffff0000, v100
	v_lshlrev_b32_e32 v142, 16, v101
	v_and_b32_e32 v143, 0xffff0000, v101
	v_lshlrev_b32_e32 v144, 16, v104
	v_and_b32_e32 v145, 0xffff0000, v104
	v_lshlrev_b32_e32 v146, 16, v105
	v_and_b32_e32 v147, 0xffff0000, v105
	v_lshlrev_b32_e32 v138, 16, v92
	v_and_b32_e32 v139, 0xffff0000, v92
	v_lshlrev_b32_e32 v136, 16, v93
	v_and_b32_e32 v137, 0xffff0000, v93
	v_pk_add_f32 v[140:141], v[140:141], v[144:145]
	v_pk_add_f32 v[142:143], v[142:143], v[146:147]
	v_pk_add_f32 v[138:139], v[140:141], v[138:139]
	v_pk_add_f32 v[136:137], v[142:143], v[136:137]
	v_mul_f32_e32 v140, v139, v139
	v_mul_f32_e32 v141, v137, v137
	v_fmac_f32_e32 v140, v138, v138
	v_fmac_f32_e32 v141, v136, v136
	v_add_f32_e32 v140, v140, v141
	v_add_f32_e32 v152, v140, v148
	v_lshlrev_b32_e32 v144, 16, v106
	v_and_b32_e32 v145, 0xffff0000, v106
	v_lshlrev_b32_e32 v146, 16, v107
	v_and_b32_e32 v147, 0xffff0000, v107
	v_lshlrev_b32_e32 v148, 16, v112
	v_and_b32_e32 v149, 0xffff0000, v112
	v_lshlrev_b32_e32 v150, 16, v113
	v_and_b32_e32 v151, 0xffff0000, v113
	v_lshlrev_b32_e32 v142, 16, v96
	v_and_b32_e32 v143, 0xffff0000, v96
	v_lshlrev_b32_e32 v140, 16, v97
	v_and_b32_e32 v141, 0xffff0000, v97
	v_pk_add_f32 v[144:145], v[144:145], v[148:149]
	v_pk_add_f32 v[146:147], v[146:147], v[150:151]
	v_pk_add_f32 v[142:143], v[144:145], v[142:143]
	v_pk_add_f32 v[140:141], v[146:147], v[140:141]
	v_mul_f32_e32 v144, v143, v143
	v_mul_f32_e32 v145, v141, v141
	v_fmac_f32_e32 v144, v142, v142
	v_fmac_f32_e32 v145, v140, v140
	v_add_f32_e32 v144, v144, v145
	v_lshlrev_b32_e32 v148, 16, v108
	v_and_b32_e32 v149, 0xffff0000, v108
	v_lshlrev_b32_e32 v150, 16, v109
	v_and_b32_e32 v151, 0xffff0000, v109
	v_lshlrev_b32_e32 v154, 16, v116
	v_and_b32_e32 v155, 0xffff0000, v116
	v_lshlrev_b32_e32 v156, 16, v117
	v_and_b32_e32 v157, 0xffff0000, v117
	v_add_f32_e32 v152, v144, v152
	v_lshlrev_b32_e32 v146, 16, v102
	v_and_b32_e32 v147, 0xffff0000, v102
	v_lshlrev_b32_e32 v144, 16, v103
	v_and_b32_e32 v145, 0xffff0000, v103
	v_pk_add_f32 v[148:149], v[148:149], v[154:155]
	v_pk_add_f32 v[150:151], v[150:151], v[156:157]
	v_pk_add_f32 v[146:147], v[148:149], v[146:147]
	v_pk_add_f32 v[144:145], v[150:151], v[144:145]
	v_mul_f32_e32 v148, v147, v147
	v_mul_f32_e32 v149, v145, v145
	v_fmac_f32_e32 v148, v146, v146
	v_fmac_f32_e32 v149, v144, v144
	v_add_f32_e32 v148, v148, v149
	v_lshlrev_b32_e32 v154, 16, v114
	v_and_b32_e32 v155, 0xffff0000, v114
	v_lshlrev_b32_e32 v156, 16, v115
	v_and_b32_e32 v157, 0xffff0000, v115
	v_lshlrev_b32_e32 v158, 16, v118
	v_and_b32_e32 v159, 0xffff0000, v118
	v_lshlrev_b32_e32 v160, 16, v119
	v_and_b32_e32 v161, 0xffff0000, v119
	v_add_f32_e32 v152, v148, v152
	v_lshlrev_b32_e32 v150, 16, v110
	v_and_b32_e32 v151, 0xffff0000, v110
	v_lshlrev_b32_e32 v148, 16, v111
	v_and_b32_e32 v149, 0xffff0000, v111
	v_pk_add_f32 v[154:155], v[154:155], v[158:159]
	v_pk_add_f32 v[156:157], v[156:157], v[160:161]
	v_pk_add_f32 v[150:151], v[154:155], v[150:151]
	v_pk_add_f32 v[148:149], v[156:157], v[148:149]
	v_mul_f32_e32 v154, v151, v151
	v_mul_f32_e32 v155, v149, v149
	v_fmac_f32_e32 v154, v150, v150
	v_fmac_f32_e32 v155, v148, v148
	v_add_f32_e32 v154, v154, v155
	v_add_f32_e32 v152, v154, v152
	ds_bpermute_b32 v154, v1, v152
	v_readlane_b32 s10, v253, 24
	v_readlane_b32 s11, v253, 25
	s_waitcnt lgkmcnt(0)
	v_add_f32_e32 v152, v152, v154
	ds_bpermute_b32 v154, v41, v152
	s_waitcnt lgkmcnt(0)
	v_add_f32_e32 v152, v152, v154
	ds_bpermute_b32 v154, v45, v152
	s_waitcnt lgkmcnt(0)
	v_add_f32_e32 v152, v152, v154
	ds_bpermute_b32 v154, v49, v152
	s_waitcnt lgkmcnt(0)
	v_add_f32_e32 v152, v152, v154
	ds_bpermute_b32 v154, v53, v152
	s_waitcnt lgkmcnt(0)
	v_add_f32_e32 v152, v152, v154
	ds_bpermute_b32 v154, v153, v152
	s_waitcnt lgkmcnt(0)
	v_add_f32_e32 v152, v152, v154
	v_fmamk_f32 v152, v152, 0x3a000000, v189
	v_mul_f32_e32 v154, 0x4f800000, v152
	v_cmp_gt_f32_e32 vcc, s84, v152
	s_nop 1
	v_cndmask_b32_e32 v152, v152, v154, vcc
	v_sqrt_f32_e32 v154, v152
	s_nop 0
	v_add_u32_e32 v155, -1, v154
	v_fma_f32 v156, -v155, v154, v152
	v_cmp_ge_f32_e64 s[36:37], 0, v156
	v_add_u32_e32 v156, 1, v154
	s_nop 0
	v_cndmask_b32_e64 v155, v154, v155, s[36:37]
	v_fma_f32 v154, -v156, v154, v152
	v_cmp_lt_f32_e64 s[36:37], 0, v154
	s_nop 1
	v_cndmask_b32_e64 v154, v155, v156, s[36:37]
	v_mul_f32_e32 v155, 0x37800000, v154
	v_cndmask_b32_e32 v154, v154, v155, vcc
	v_cmp_class_f32_e32 vcc, v152, v190
	s_nop 1
	v_cndmask_b32_e32 v152, v154, v152, vcc
	v_div_scale_f32 v154, s[8:9], v152, v152, 1.0
	v_rcp_f32_e32 v155, v154
	s_mov_b64 s[8:9], -1
	v_fma_f32 v156, -v154, v155, 1.0
	v_fmac_f32_e32 v155, v156, v155
	v_div_scale_f32 v156, vcc, 1.0, v152, 1.0
	v_mul_f32_e32 v157, v156, v155
	v_fma_f32 v158, -v154, v157, v156
	v_fmac_f32_e32 v157, v158, v155
	v_fma_f32 v154, -v154, v157, v156
	v_div_fmas_f32 v154, v154, v155, v157
	v_div_fixup_f32 v152, v154, v152, 1.0
	s_and_b64 vcc, exec, s[10:11]
	s_cbranch_vccz .LBB0_1878
	v_max_f32_e64 v154, |v125|, |v125|
	v_max_f32_e64 v155, |v124|, |v124|
	v_max_f32_e32 v154, v155, v154
	v_max_f32_e64 v155, |v121|, |v121|
	v_max_f32_e64 v156, |v120|, |v120|
	v_max_f32_e32 v155, v156, v155
	v_max3_f32 v154, |v126|, |v127|, v154
	v_max3_f32 v155, |v122|, |v123|, v155
	v_max3_f32 v154, v154, 0, v155
	v_max_f32_e64 v155, |v129|, |v129|
	v_max_f32_e64 v156, |v128|, |v128|
	v_max_f32_e32 v155, v156, v155
	v_max_f32_e64 v156, |v133|, |v133|
	v_max_f32_e64 v157, |v132|, |v132|
	v_max_f32_e32 v156, v157, v156
	v_max3_f32 v155, |v130|, |v131|, v155
	v_max3_f32 v156, |v134|, |v135|, v156
	v_max3_f32 v154, v154, v155, v156
	v_max_f32_e64 v155, |v137|, |v137|
	v_max_f32_e64 v156, |v136|, |v136|
	v_max_f32_e32 v155, v156, v155
	v_max_f32_e64 v156, |v141|, |v141|
	v_max_f32_e64 v157, |v140|, |v140|
	v_max_f32_e32 v156, v157, v156
	v_max3_f32 v155, |v138|, |v139|, v155
	v_max3_f32 v156, |v142|, |v143|, v156
	v_max3_f32 v154, v154, v155, v156
	v_max_f32_e64 v155, |v145|, |v145|
	v_max_f32_e64 v156, |v144|, |v144|
	v_max_f32_e32 v155, v156, v155
	v_max_f32_e64 v156, |v149|, |v149|
	v_max_f32_e64 v157, |v148|, |v148|
	v_max_f32_e32 v156, v157, v156
	v_max3_f32 v155, |v146|, |v147|, v155
	v_max3_f32 v156, |v150|, |v151|, v156
	v_max3_f32 v154, v154, v155, v156
	ds_bpermute_b32 v155, v1, v154
	s_ashr_i32 s3, s2, 31
	s_waitcnt lgkmcnt(0)
	v_max_f32_e32 v155, v155, v155
	v_max_f32_e32 v154, v154, v155
	ds_bpermute_b32 v155, v41, v154
	s_waitcnt lgkmcnt(0)
	v_max_f32_e32 v155, v155, v155
	v_max_f32_e32 v154, v154, v155
	ds_bpermute_b32 v155, v45, v154
	s_waitcnt lgkmcnt(0)
	v_max_f32_e32 v155, v155, v155
	v_max_f32_e32 v154, v154, v155
	ds_bpermute_b32 v155, v49, v154
	s_waitcnt lgkmcnt(0)
	v_max_f32_e32 v155, v155, v155
	v_max_f32_e32 v154, v154, v155
	ds_bpermute_b32 v155, v53, v154
	s_waitcnt lgkmcnt(0)
	v_max_f32_e32 v155, v155, v155
	v_max_f32_e32 v154, v154, v155
	ds_bpermute_b32 v155, v153, v154
	s_waitcnt lgkmcnt(0)
	v_max_f32_e32 v155, v155, v155
	v_max_f32_e32 v154, v154, v155
	v_mul_f32_e32 v154, v152, v154
	v_max_f32_e32 v154, 0x1e3ce508, v154
	s_and_saveexec_b64 s[8:9], s[34:35]
	s_cbranch_execz .LBB0_1877
	s_lshl_b64 s[10:11], s[2:3], 2
	v_readlane_b32 s12, v253, 26
	v_readlane_b32 s13, v253, 27
	s_add_u32 s10, s12, s10
	s_addc_u32 s11, s13, s11
	v_mul_f32_e32 v155, 0x3c010204, v154
	global_store_dword v173, v155, s[10:11] nt
.LBB0_1877:
	s_or_b64 exec, exec, s[8:9]
	v_mul_f32_e32 v155, 0x42fe0000, v152
	v_div_scale_f32 v156, s[8:9], v154, v154, v155
	v_rcp_f32_e32 v157, v156
	v_div_scale_f32 v158, vcc, v155, v154, v155
	s_lshl_b64 s[8:9], s[2:3], 11
	v_fma_f32 v159, -v156, v157, 1.0
	v_fmac_f32_e32 v157, v159, v157
	v_mul_f32_e32 v159, v158, v157
	v_fma_f32 v160, -v156, v159, v158
	v_fmac_f32_e32 v159, v160, v157
	v_fma_f32 v156, -v156, v159, v158
	v_div_fmas_f32 v156, v156, v157, v159
	v_div_fixup_f32 v154, v156, v154, v155
	v_lshl_add_u64 v[156:157], v[26:27], 0, s[8:9]
	s_lshl_b64 s[8:9], s[2:3], 12
	v_cvt_pk_bf16_f32 v158, v126, v127
	v_cvt_pk_bf16_f32 v159, v124, v125
	v_lshl_add_u64 v[160:161], v[32:33], 0, s[8:9]
	v_pk_mul_f32 v[162:163], v[126:127], v[154:155] op_sel_hi:[1,0]
	global_store_dwordx2 v[160:161], v[158:159], off nt
	v_pk_mul_f32 v[158:159], v[124:125], v[154:155] op_sel_hi:[1,0]
	v_rndne_f32_e32 v155, v162
	v_rndne_f32_e32 v162, v163
	v_cvt_i32_f32_e32 v162, v162
	v_rndne_f32_e32 v158, v158
	v_rndne_f32_e32 v159, v159
	v_cvt_i32_f32_e32 v155, v155
	v_cvt_i32_f32_sdwa v158, v158 dst_sel:WORD_1 dst_unused:UNUSED_PAD src0_sel:DWORD
	v_cvt_i32_f32_e32 v159, v159
	v_lshlrev_b32_e32 v162, 8, v162
	v_and_b32_e32 v162, 0xff00, v162
	v_and_b32_e32 v158, 0xff0000, v158
	v_perm_b32 v155, v159, v155, s89
	v_or3_b32 v155, v155, v162, v158
	global_store_dword v[156:157], v155, off nt
	v_cvt_pk_bf16_f32 v158, v122, v123
	v_cvt_pk_bf16_f32 v159, v120, v121
	v_pk_mul_f32 v[162:163], v[122:123], v[154:155] op_sel_hi:[1,0]
	global_store_dwordx2 v[160:161], v[158:159], off offset:512 nt
	v_pk_mul_f32 v[158:159], v[120:121], v[154:155] op_sel_hi:[1,0]
	v_rndne_f32_e32 v155, v162
	v_rndne_f32_e32 v162, v163
	v_cvt_i32_f32_e32 v162, v162
	v_rndne_f32_e32 v158, v158
	v_rndne_f32_e32 v159, v159
	v_cvt_i32_f32_e32 v155, v155
	v_cvt_i32_f32_sdwa v158, v158 dst_sel:WORD_1 dst_unused:UNUSED_PAD src0_sel:DWORD
	v_cvt_i32_f32_e32 v159, v159
	v_lshlrev_b32_e32 v162, 8, v162
	v_and_b32_e32 v162, 0xff00, v162
	v_and_b32_e32 v158, 0xff0000, v158
	v_perm_b32 v155, v159, v155, s89
	v_or3_b32 v155, v155, v162, v158
	global_store_dword v[156:157], v155, off offset:256 nt
	v_cvt_pk_bf16_f32 v158, v130, v131
	v_cvt_pk_bf16_f32 v159, v128, v129
	v_pk_mul_f32 v[162:163], v[130:131], v[154:155] op_sel_hi:[1,0]
	global_store_dwordx2 v[160:161], v[158:159], off offset:1024 nt
	v_pk_mul_f32 v[158:159], v[128:129], v[154:155] op_sel_hi:[1,0]
	v_rndne_f32_e32 v155, v162
	v_rndne_f32_e32 v162, v163
	v_cvt_i32_f32_e32 v162, v162
	v_rndne_f32_e32 v158, v158
	v_rndne_f32_e32 v159, v159
	v_cvt_i32_f32_e32 v155, v155
	v_cvt_i32_f32_sdwa v158, v158 dst_sel:WORD_1 dst_unused:UNUSED_PAD src0_sel:DWORD
	v_cvt_i32_f32_e32 v159, v159
	v_lshlrev_b32_e32 v162, 8, v162
	v_and_b32_e32 v162, 0xff00, v162
	v_and_b32_e32 v158, 0xff0000, v158
	v_perm_b32 v155, v159, v155, s89
	v_or3_b32 v155, v155, v162, v158
	global_store_dword v[156:157], v155, off offset:512 nt
	v_cvt_pk_bf16_f32 v158, v134, v135
	v_cvt_pk_bf16_f32 v159, v132, v133
	v_pk_mul_f32 v[162:163], v[134:135], v[154:155] op_sel_hi:[1,0]
	global_store_dwordx2 v[160:161], v[158:159], off offset:1536 nt
	v_pk_mul_f32 v[158:159], v[132:133], v[154:155] op_sel_hi:[1,0]
	v_rndne_f32_e32 v155, v162
	v_rndne_f32_e32 v162, v163
	v_cvt_i32_f32_e32 v162, v162
	v_rndne_f32_e32 v158, v158
	v_rndne_f32_e32 v159, v159
	v_cvt_i32_f32_e32 v155, v155
	v_cvt_i32_f32_sdwa v158, v158 dst_sel:WORD_1 dst_unused:UNUSED_PAD src0_sel:DWORD
	v_cvt_i32_f32_e32 v159, v159
	v_lshlrev_b32_e32 v162, 8, v162
	v_and_b32_e32 v162, 0xff00, v162
	v_and_b32_e32 v158, 0xff0000, v158
	v_perm_b32 v155, v159, v155, s89
	v_or3_b32 v155, v155, v162, v158
	global_store_dword v[156:157], v155, off offset:768 nt
	v_cvt_pk_bf16_f32 v158, v138, v139
	v_cvt_pk_bf16_f32 v159, v136, v137
	v_pk_mul_f32 v[162:163], v[138:139], v[154:155] op_sel_hi:[1,0]
	global_store_dwordx2 v[160:161], v[158:159], off offset:2048 nt
	v_pk_mul_f32 v[158:159], v[136:137], v[154:155] op_sel_hi:[1,0]
	v_rndne_f32_e32 v155, v162
	v_rndne_f32_e32 v162, v163
	v_cvt_i32_f32_e32 v162, v162
	v_rndne_f32_e32 v158, v158
	v_rndne_f32_e32 v159, v159
	v_cvt_i32_f32_e32 v155, v155
	v_cvt_i32_f32_sdwa v158, v158 dst_sel:WORD_1 dst_unused:UNUSED_PAD src0_sel:DWORD
	v_cvt_i32_f32_e32 v159, v159
	v_lshlrev_b32_e32 v162, 8, v162
	v_and_b32_e32 v162, 0xff00, v162
	v_and_b32_e32 v158, 0xff0000, v158
	v_perm_b32 v155, v159, v155, s89
	v_or3_b32 v155, v155, v162, v158
	global_store_dword v[156:157], v155, off offset:1024 nt
	v_cvt_pk_bf16_f32 v158, v142, v143
	v_cvt_pk_bf16_f32 v159, v140, v141
	v_pk_mul_f32 v[162:163], v[142:143], v[154:155] op_sel_hi:[1,0]
	global_store_dwordx2 v[160:161], v[158:159], off offset:2560 nt
	v_pk_mul_f32 v[158:159], v[140:141], v[154:155] op_sel_hi:[1,0]
	v_rndne_f32_e32 v155, v162
	v_rndne_f32_e32 v162, v163
	v_cvt_i32_f32_e32 v162, v162
	v_rndne_f32_e32 v158, v158
	v_rndne_f32_e32 v159, v159
	v_cvt_i32_f32_e32 v155, v155
	v_cvt_i32_f32_sdwa v158, v158 dst_sel:WORD_1 dst_unused:UNUSED_PAD src0_sel:DWORD
	v_cvt_i32_f32_e32 v159, v159
	v_lshlrev_b32_e32 v162, 8, v162
	v_and_b32_e32 v162, 0xff00, v162
	v_and_b32_e32 v158, 0xff0000, v158
	v_perm_b32 v155, v159, v155, s89
	v_or3_b32 v155, v155, v162, v158
	global_store_dword v[156:157], v155, off offset:1280 nt
	v_cvt_pk_bf16_f32 v158, v146, v147
	v_cvt_pk_bf16_f32 v159, v144, v145
	v_pk_mul_f32 v[162:163], v[146:147], v[154:155] op_sel_hi:[1,0]
	global_store_dwordx2 v[160:161], v[158:159], off offset:3072 nt
	v_pk_mul_f32 v[158:159], v[144:145], v[154:155] op_sel_hi:[1,0]
	v_rndne_f32_e32 v155, v162
	v_rndne_f32_e32 v162, v163
	v_cvt_i32_f32_e32 v162, v162
	v_rndne_f32_e32 v158, v158
	v_rndne_f32_e32 v159, v159
	v_cvt_i32_f32_e32 v155, v155
	v_cvt_i32_f32_sdwa v158, v158 dst_sel:WORD_1 dst_unused:UNUSED_PAD src0_sel:DWORD
	v_cvt_i32_f32_e32 v159, v159
	v_lshlrev_b32_e32 v162, 8, v162
	v_and_b32_e32 v162, 0xff00, v162
	v_and_b32_e32 v158, 0xff0000, v158
	v_perm_b32 v155, v159, v155, s89
	v_or3_b32 v155, v155, v162, v158
	global_store_dword v[156:157], v155, off offset:1536 nt
	v_cvt_pk_bf16_f32 v158, v150, v151
	v_cvt_pk_bf16_f32 v159, v148, v149
	global_store_dwordx2 v[160:161], v[158:159], off offset:3584 nt
	v_pk_mul_f32 v[158:159], v[148:149], v[154:155] op_sel_hi:[1,0]
	v_pk_mul_f32 v[154:155], v[150:151], v[154:155] op_sel_hi:[1,0]
	v_rndne_f32_e32 v158, v158
	v_rndne_f32_e32 v155, v155
	v_rndne_f32_e32 v154, v154
	v_cvt_i32_f32_e32 v155, v155
	v_rndne_f32_e32 v159, v159
	v_cvt_i32_f32_e32 v154, v154
	v_cvt_i32_f32_sdwa v158, v158 dst_sel:WORD_1 dst_unused:UNUSED_PAD src0_sel:DWORD
	v_cvt_i32_f32_e32 v159, v159
	v_lshlrev_b32_e32 v155, 8, v155
	v_and_b32_e32 v155, 0xff00, v155
	v_and_b32_e32 v158, 0xff0000, v158
	v_perm_b32 v154, v159, v154, s89
	v_or3_b32 v154, v154, v155, v158
	s_mov_b64 s[8:9], 0
	global_store_dword v[156:157], v154, off offset:1792 nt
.LBB0_1878:
	s_and_b64 vcc, exec, s[8:9]
	s_cbranch_vccz .LBB0_1861
	global_load_dwordx4 v[154:157], v[38:39], off
	s_ashr_i32 s3, s2, 31
	v_readlane_b32 s36, v252, 24
	s_lshl_b64 s[8:9], s[2:3], 13
	v_readlane_b32 s48, v252, 36
	v_readlane_b32 s49, v252, 37
	s_add_u32 s8, s48, s8
	v_pk_mul_f32 v[124:125], v[124:125], v[152:153] op_sel_hi:[1,0]
	v_pk_mul_f32 v[158:159], v[126:127], v[152:153] op_sel_hi:[1,0]
	s_addc_u32 s9, s49, s9
	v_pk_mul_f32 v[120:121], v[120:121], v[152:153] op_sel_hi:[1,0]
	v_readlane_b32 s37, v252, 25
	v_readlane_b32 s38, v252, 26
	v_readlane_b32 s39, v252, 27
	v_readlane_b32 s40, v252, 28
	v_readlane_b32 s41, v252, 29
	v_readlane_b32 s42, v252, 30
	v_readlane_b32 s43, v252, 31
	v_readlane_b32 s44, v252, 32
	v_readlane_b32 s45, v252, 33
	v_readlane_b32 s46, v252, 34
	v_readlane_b32 s47, v252, 35
	v_readlane_b32 s50, v252, 38
	v_readlane_b32 s51, v252, 39
	s_waitcnt vmcnt(0)
	v_pk_mul_f32 v[126:127], v[124:125], v[156:157]
	v_pk_mul_f32 v[124:125], v[158:159], v[154:155]
	v_lshlrev_b32_e32 v156, 4, v0
	global_store_dwordx4 v156, v[124:127], s[8:9] nt
	global_load_dwordx4 v[124:127], v[38:39], off offset:1024
	v_pk_mul_f32 v[154:155], v[122:123], v[152:153] op_sel_hi:[1,0]
	s_waitcnt vmcnt(0)
	v_pk_mul_f32 v[122:123], v[120:121], v[126:127]
	v_pk_mul_f32 v[120:121], v[154:155], v[124:125]
	global_store_dwordx4 v156, v[120:123], s[8:9] offset:1024 nt
	global_load_dwordx4 v[120:123], v[38:39], off offset:2048
	v_pk_mul_f32 v[124:125], v[128:129], v[152:153] op_sel_hi:[1,0]
	v_pk_mul_f32 v[126:127], v[130:131], v[152:153] op_sel_hi:[1,0]
	s_waitcnt vmcnt(0)
	v_pk_mul_f32 v[122:123], v[124:125], v[122:123]
	v_pk_mul_f32 v[120:121], v[126:127], v[120:121]
	global_store_dwordx4 v156, v[120:123], s[8:9] offset:2048 nt
	global_load_dwordx4 v[120:123], v[38:39], off offset:3072
	v_pk_mul_f32 v[124:125], v[132:133], v[152:153] op_sel_hi:[1,0]
	v_pk_mul_f32 v[126:127], v[134:135], v[152:153] op_sel_hi:[1,0]
	s_waitcnt vmcnt(0)
	v_pk_mul_f32 v[122:123], v[124:125], v[122:123]
	v_pk_mul_f32 v[120:121], v[126:127], v[120:121]
	global_store_dwordx4 v156, v[120:123], s[8:9] offset:3072 nt
	global_load_dwordx4 v[120:123], v[42:43], off
	v_pk_mul_f32 v[124:125], v[136:137], v[152:153] op_sel_hi:[1,0]
	v_pk_mul_f32 v[126:127], v[138:139], v[152:153] op_sel_hi:[1,0]
	s_waitcnt vmcnt(0)
	v_pk_mul_f32 v[122:123], v[124:125], v[122:123]
	v_pk_mul_f32 v[120:121], v[126:127], v[120:121]
	v_lshlrev_b32_e32 v124, 4, v40
	global_store_dwordx4 v124, v[120:123], s[8:9] nt
	global_load_dwordx4 v[120:123], v[46:47], off
	v_pk_mul_f32 v[124:125], v[140:141], v[152:153] op_sel_hi:[1,0]
	v_pk_mul_f32 v[126:127], v[142:143], v[152:153] op_sel_hi:[1,0]
	s_waitcnt vmcnt(0)
	v_pk_mul_f32 v[122:123], v[124:125], v[122:123]
	v_pk_mul_f32 v[120:121], v[126:127], v[120:121]
	v_lshlrev_b32_e32 v124, 4, v44
	global_store_dwordx4 v124, v[120:123], s[8:9] nt
	global_load_dwordx4 v[120:123], v[50:51], off
	v_pk_mul_f32 v[124:125], v[144:145], v[152:153] op_sel_hi:[1,0]
	v_pk_mul_f32 v[126:127], v[146:147], v[152:153] op_sel_hi:[1,0]
	s_waitcnt vmcnt(0)
	v_pk_mul_f32 v[122:123], v[124:125], v[122:123]
	v_pk_mul_f32 v[120:121], v[126:127], v[120:121]
	v_lshlrev_b32_e32 v124, 4, v48
	global_store_dwordx4 v124, v[120:123], s[8:9] nt
	global_load_dwordx4 v[120:123], v[58:59], off
	v_pk_mul_f32 v[124:125], v[148:149], v[152:153] op_sel_hi:[1,0]
	v_pk_mul_f32 v[126:127], v[150:151], v[152:153] op_sel_hi:[1,0]
	s_waitcnt vmcnt(0)
	v_pk_mul_f32 v[122:123], v[124:125], v[122:123]
	v_pk_mul_f32 v[120:121], v[126:127], v[120:121]
	v_lshlrev_b32_e32 v124, 4, v52
	global_store_dwordx4 v124, v[120:123], s[8:9] nt
	s_branch .LBB0_1861
